# all six GEMM instances: first K-loop iteration of each unit peeled with C=0 on each accumulator's first MFMA, removing the 128-instruction accumulator zeroing per unit
# speedup vs baseline: 1.0139x; 1.0056x over previous
; #define PG8_STAGE(bufoff, gbase, voff) do { _Pragma("unroll") for (int _i = 0; _i < 2; ++_i) \
;         __builtin_amdgcn_global_load_lds((const unsigned*)((const char*)(gbase) + (voff)[_i]), (LAS unsigned*)(lds + (bufoff) + ldsw + _i * 8192), 16, 0, 0); } while (0)
; #define PG8_LDA(dst, b, h) do { _Pragma("unroll") for (int m = 0; m < 4; ++m) _Pragma("unroll") for (int k = 0; k < 2; ++k) dst[m][k] = *(const LAS bf16x8*)(lds + PG8_SA(b, h) + aoff + m * 2048 + k * KOFF); } while (0)
; #define PG8_LDB(dst, b, h) do { _Pragma("unroll") for (int n = 0; n < 2; ++n) _Pragma("unroll") for (int k = 0; k < 2; ++k) dst[n][k] = *(const LAS bf16x8*)(lds + PG8_SB(b, h) + boff + n * 2048 + k * KOFF); } while (0)
; #define PG8_WAIT_V(n) asm volatile("s_waitcnt vmcnt(" #n ")" ::: "memory")
; #define PG8_WAIT_L(n) asm volatile("s_waitcnt lgkmcnt(" #n ")" ::: "memory")
; #define PG8_BAR __builtin_amdgcn_s_barrier()
; #define PG8_SCHED __builtin_amdgcn_sched_barrier(0)
; #define PG8_AOFF(u_, o0, o1) do { _Pragma("unroll") for (int _i = 0; _i < 2; ++_i) { const int r0 = (u_).pm * BM + Rr[_i], r1 = r0 + HALF; \
;         const int g0 = GATHER ? g.rowidx[r0] : r0, g1 = GATHER ? g.rowidx[r1] : r1; \
;         o0[_i] = (unsigned)g0 * (unsigned)K + (unsigned)Cc[_i]; o1[_i] = (unsigned)g1 * (unsigned)K + (unsigned)Cc[_i]; } } while (0)
; template <class Epi, class Sched, bool GATHER, bool FP8 = false, bool ALIGN = true>
; __device__ __forceinline__ void gemm_phase(LAS unsigned char* lds, int wave, const Gemm g, const Sched& S, const Epi& E) {
;     ...
;             PG8_LDB(B0, 0, 0); PG8_LDB(B1, 0, 1); PG8_SCHED; PG8_LDA(At, 0, 0); PG8_STAGE(PG8_SA(1, 1), a1, ca1);
;             if (last && has_next) PG8_AOFF(nxt, ca0, ca1);
;             PG8_WAIT_V(8); PG8_WAIT_L(0); PG8_BAR; PG8_MMA(0, 0, At, B0); PG8_MMA(0, 1, At, B1); PG8_BAR; PG8_SCHED;
;             PG8_LDA(At, 0, 1); PG8_STAGE(PG8_SB(0, 0), b2, voffB0); PG8_STAGE(PG8_SB(0, 1), b2, voffB1); PG8_STAGE(PG8_SA(0, 0), a2, ca0);
;             PG8_WAIT_V(8); PG8_WAIT_L(0); PG8_BAR; PG8_MMA(1, 0, At, B0); PG8_MMA(1, 1, At, B1); PG8_BAR; PG8_SCHED;
;     ...
; #pragma unroll
;         for (int a = 0; a < 2; ++a)
; #pragma unroll
;             for (int b = 0; b < 2; ++b)
; #pragma unroll
;                 for (int m = 0; m < 4; ++m)
; #pragma unroll
;                     for (int n = 0; n < 2; ++n) acc[a][b][m][n] = (f32x4){0.f, 0.f, 0.f, 0.f};
.LBB0_254:
	s_ashr_i32 s49, s48, 31
	s_lshl_b64 s[12:13], s[48:49], 20
	s_add_u32 s50, s34, s12
	s_addc_u32 s51, s35, s13
	s_and_b64 s[12:13], s[40:41], exec
	s_cselect_b32 s49, s51, s81
	s_cselect_b32 s92, s50, s80
	s_lshl_b32 s12, s90, 20
	v_add_u32_e32 v241, s12, v235
	v_add_u32_e32 v242, s12, v236
	s_add_u32 s93, s80, 0x100
	v_add_u32_e32 v218, 0x80000, v241
	v_add_u32_e32 v220, 0x80000, v242
	v_mov_b32_e32 v219, v193
	v_mov_b32_e32 v221, v193
	s_addc_u32 s94, s81, 0
	s_mov_b32 s95, -2
	s_mov_b64 s[80:81], s[6:7]
.Lpeel_p0_h:
	v_add_u32_e32 v128, 0, v238
	v_add_u32_e32 v129, 0x10000, v128
	v_add_u32_e32 v140, 0x14000, v128
	ds_read_b128 v[144:147], v129
	ds_read_b128 v[148:151], v129 offset:1024
	ds_read_b128 v[152:155], v129 offset:2048
	ds_read_b128 v[156:159], v129 offset:3072
	ds_read_b128 v[128:131], v140
	ds_read_b128 v[132:135], v140 offset:1024
	ds_read_b128 v[136:139], v140 offset:2048
	ds_read_b128 v[140:143], v140 offset:3072
	s_cmp_eq_u32 s95, 28
	s_cselect_b64 s[12:13], -1, 0
	s_add_i32 m0, s57, 0xc000
	ds_read_b128 v[184:187], v240
	ds_read_b128 v[188:191], v240 offset:1024
	ds_read_b128 v[176:179], v240 offset:2048
	ds_read_b128 v[180:183], v240 offset:3072
	ds_read_b128 v[168:171], v240 offset:4096
	ds_read_b128 v[172:175], v240 offset:5120
	ds_read_b128 v[160:163], v240 offset:6144
	ds_read_b128 v[164:167], v240 offset:7168
	global_load_lds_dwordx4 v214, s[80:81]
	s_add_i32 m0, s57, 0xe000
	s_and_b64 s[96:97], s[40:41], s[12:13]
	global_load_lds_dwordx4 v216, s[80:81]
	s_andn2_b64 vcc, exec, s[96:97]
	s_cbranch_vccz .Lpeel_p0_a
	v_mov_b32_e32 v215, v193
	v_mov_b32_e32 v217, v193
	v_mov_b64_e32 v[222:223], v[216:217]
	v_mov_b64_e32 v[224:225], v[214:215]
	s_branch .Lpeel_p0_b
.Lpeel_p0_a:
	v_mov_b64_e32 v[222:223], v[220:221]
	v_mov_b64_e32 v[224:225], v[218:219]
	v_mov_b32_e32 v212, v242
	v_mov_b32_e32 v192, v241
	v_mov_b32_e32 v216, v220
	v_mov_b32_e32 v214, v218
.Lpeel_p0_b:
	s_waitcnt vmcnt(8)
	s_add_u32 s96, s80, 0x80
	s_waitcnt lgkmcnt(0)
	s_addc_u32 s97, s81, 0
	s_and_b64 s[12:13], s[12:13], exec
	s_cselect_b32 s13, s5, s97
	s_cselect_b32 s12, s4, s96
	s_cselect_b32 s97, s49, s94
	s_cselect_b32 s96, s92, s93
	s_barrier
	s_setprio 1
	s_waitcnt lgkmcnt(0)
	v_mfma_f32_16x16x32_bf16 v[124:127], v[144:147], v[184:187], 0
	v_mfma_f32_16x16x32_bf16 v[120:123], v[152:155], v[184:187], 0
	v_mfma_f32_16x16x32_bf16 v[116:119], v[144:147], v[176:179], 0
	v_mfma_f32_16x16x32_bf16 v[112:115], v[152:155], v[176:179], 0
	v_mfma_f32_16x16x32_bf16 v[100:103], v[144:147], v[168:171], 0
	v_mfma_f32_16x16x32_bf16 v[96:99], v[152:155], v[168:171], 0
	v_mfma_f32_16x16x32_bf16 v[84:87], v[144:147], v[160:163], 0
	v_mfma_f32_16x16x32_bf16 v[80:83], v[152:155], v[160:163], 0
	v_mfma_f32_16x16x32_bf16 v[124:127], v[148:151], v[188:191], v[124:127]
	v_mfma_f32_16x16x32_bf16 v[120:123], v[156:159], v[188:191], v[120:123]
	v_mfma_f32_16x16x32_bf16 v[116:119], v[148:151], v[180:183], v[116:119]
	v_mfma_f32_16x16x32_bf16 v[112:115], v[156:159], v[180:183], v[112:115]
	v_mfma_f32_16x16x32_bf16 v[100:103], v[148:151], v[172:175], v[100:103]
	v_mfma_f32_16x16x32_bf16 v[96:99], v[156:159], v[172:175], v[96:99]
	v_mfma_f32_16x16x32_bf16 v[84:87], v[148:151], v[164:167], v[84:87]
	v_mfma_f32_16x16x32_bf16 v[80:83], v[156:159], v[164:167], v[80:83]
	s_setprio 0
	s_setprio 1
	v_mfma_f32_16x16x32_bf16 v[108:111], v[128:131], v[184:187], 0
	v_mfma_f32_16x16x32_bf16 v[104:107], v[136:139], v[184:187], 0
	v_mfma_f32_16x16x32_bf16 v[92:95], v[128:131], v[176:179], 0
	v_mfma_f32_16x16x32_bf16 v[88:91], v[136:139], v[176:179], 0
	v_mfma_f32_16x16x32_bf16 v[76:79], v[128:131], v[168:171], 0
	v_mfma_f32_16x16x32_bf16 v[72:75], v[136:139], v[168:171], 0
	v_mfma_f32_16x16x32_bf16 v[68:71], v[128:131], v[160:163], 0
	v_mfma_f32_16x16x32_bf16 v[64:67], v[136:139], v[160:163], 0
	v_mfma_f32_16x16x32_bf16 v[108:111], v[132:135], v[188:191], v[108:111]
	v_mfma_f32_16x16x32_bf16 v[104:107], v[140:143], v[188:191], v[104:107]
	v_mfma_f32_16x16x32_bf16 v[92:95], v[132:135], v[180:183], v[92:95]
	v_mfma_f32_16x16x32_bf16 v[88:91], v[140:143], v[180:183], v[88:91]
	v_mfma_f32_16x16x32_bf16 v[76:79], v[132:135], v[172:175], v[76:79]
	v_mfma_f32_16x16x32_bf16 v[72:75], v[140:143], v[172:175], v[72:75]
	v_mfma_f32_16x16x32_bf16 v[68:71], v[132:135], v[164:167], v[68:71]
	v_mfma_f32_16x16x32_bf16 v[64:67], v[140:143], v[164:167], v[64:67]
	s_setprio 0
	s_barrier
	s_mov_b32 m0, s58
	v_lshl_add_u64 v[196:197], s[96:97], 0, v[208:209]
	ds_read_b128 v[160:163], v240 offset:16384
	ds_read_b128 v[164:167], v240 offset:17408
	ds_read_b128 v[168:171], v240 offset:18432
	ds_read_b128 v[172:175], v240 offset:19456
	ds_read_b128 v[176:179], v240 offset:20480
	ds_read_b128 v[180:183], v240 offset:21504
	ds_read_b128 v[184:187], v240 offset:22528
	ds_read_b128 v[188:191], v240 offset:23552
	global_load_lds_dwordx4 v[196:197], off
	v_lshl_add_u64 v[198:199], s[96:97], 0, v[204:205]
	s_mov_b32 m0, s59
	v_lshl_add_u64 v[200:201], s[96:97], 0, v[210:211]
	global_load_lds_dwordx4 v[198:199], off
	s_mov_b32 m0, s60
	v_lshl_add_u64 v[202:203], s[96:97], 0, v[206:207]
	global_load_lds_dwordx4 v[200:201], off
	s_mov_b32 m0, s73
	v_mov_b32_e32 v213, v193
	global_load_lds_dwordx4 v[202:203], off
	s_mov_b32 m0, s57
	v_lshl_add_u64 v[226:227], s[12:13], 0, v[192:193]
	global_load_lds_dwordx4 v192, s[12:13]
	s_mov_b32 m0, s79
	v_lshl_add_u64 v[228:229], s[12:13], 0, v[212:213]
	global_load_lds_dwordx4 v212, s[12:13]
	s_waitcnt vmcnt(8)
	s_waitcnt lgkmcnt(0)
	s_barrier
; #define PG8_STAGE(bufoff, gbase, voff) do { _Pragma("unroll") for (int _i = 0; _i < 2; ++_i) \
;         __builtin_amdgcn_global_load_lds((const unsigned*)((const char*)(gbase) + (voff)[_i]), (LAS unsigned*)(lds + (bufoff) + ldsw + _i * 8192), 16, 0, 0); } while (0)
; #define PG8_LDA(dst, b, h) do { _Pragma("unroll") for (int m = 0; m < 4; ++m) _Pragma("unroll") for (int k = 0; k < 2; ++k) dst[m][k] = *(const LAS bf16x8*)(lds + PG8_SA(b, h) + aoff + m * 2048 + k * KOFF); } while (0)
; #define PG8_LDB(dst, b, h) do { _Pragma("unroll") for (int n = 0; n < 2; ++n) _Pragma("unroll") for (int k = 0; k < 2; ++k) dst[n][k] = *(const LAS bf16x8*)(lds + PG8_SB(b, h) + boff + n * 2048 + k * KOFF); } while (0)
; #define PG8_WAIT_V(n) asm volatile("s_waitcnt vmcnt(" #n ")" ::: "memory")
; #define PG8_WAIT_L(n) asm volatile("s_waitcnt lgkmcnt(" #n ")" ::: "memory")
; #define PG8_BAR __builtin_amdgcn_s_barrier()
; #define PG8_SCHED __builtin_amdgcn_sched_barrier(0)
; template <class Epi, class Sched, bool GATHER, bool FP8 = false, bool ALIGN = true>
; __device__ __forceinline__ void gemm_phase(LAS unsigned char* lds, int wave, const Gemm g, const Sched& S, const Epi& E) {
;     ...
;             PG8_WAIT_V(8); PG8_WAIT_L(0); PG8_BAR; PG8_MMA(1, 0, At, B0); PG8_MMA(1, 1, At, B1); PG8_BAR; PG8_SCHED;
;             PG8_LDB(B0, 1, 0); PG8_LDB(B1, 1, 1); PG8_SCHED; PG8_LDA(At, 1, 0); PG8_STAGE(PG8_SA(0, 1), a2, ca1);
;             PG8_WAIT_V(8); PG8_WAIT_L(0); PG8_BAR; PG8_MMA(0, 0, At, B0); PG8_MMA(0, 1, At, B1); PG8_BAR; PG8_SCHED;
	s_setprio 1
	s_waitcnt lgkmcnt(0)
	v_mfma_f32_16x16x32_bf16 v[60:63], v[144:147], v[160:163], 0
	v_mfma_f32_16x16x32_bf16 v[56:59], v[152:155], v[160:163], 0
	v_mfma_f32_16x16x32_bf16 v[52:55], v[144:147], v[168:171], 0
	v_mfma_f32_16x16x32_bf16 v[48:51], v[152:155], v[168:171], 0
	v_mfma_f32_16x16x32_bf16 v[36:39], v[144:147], v[176:179], 0
	v_mfma_f32_16x16x32_bf16 v[32:35], v[152:155], v[176:179], 0
	v_mfma_f32_16x16x32_bf16 v[20:23], v[144:147], v[184:187], 0
	v_mfma_f32_16x16x32_bf16 v[16:19], v[152:155], v[184:187], 0
	v_mfma_f32_16x16x32_bf16 v[60:63], v[148:151], v[164:167], v[60:63]
	v_mfma_f32_16x16x32_bf16 v[56:59], v[156:159], v[164:167], v[56:59]
	v_mfma_f32_16x16x32_bf16 v[52:55], v[148:151], v[172:175], v[52:55]
	v_mfma_f32_16x16x32_bf16 v[48:51], v[156:159], v[172:175], v[48:51]
	v_mfma_f32_16x16x32_bf16 v[36:39], v[148:151], v[180:183], v[36:39]
	v_mfma_f32_16x16x32_bf16 v[32:35], v[156:159], v[180:183], v[32:35]
	v_mfma_f32_16x16x32_bf16 v[20:23], v[148:151], v[188:191], v[20:23]
	v_mfma_f32_16x16x32_bf16 v[16:19], v[156:159], v[188:191], v[16:19]
	s_setprio 0
	s_setprio 1
	v_mfma_f32_16x16x32_bf16 v[44:47], v[128:131], v[160:163], 0
	v_mfma_f32_16x16x32_bf16 v[40:43], v[136:139], v[160:163], 0
	v_mfma_f32_16x16x32_bf16 v[28:31], v[128:131], v[168:171], 0
	v_mfma_f32_16x16x32_bf16 v[24:27], v[136:139], v[168:171], 0
	v_mfma_f32_16x16x32_bf16 v[12:15], v[128:131], v[176:179], 0
	v_mfma_f32_16x16x32_bf16 v[8:11], v[136:139], v[176:179], 0
	v_mfma_f32_16x16x32_bf16 v[4:7], v[128:131], v[184:187], 0
	v_mfma_f32_16x16x32_bf16 v[0:3], v[136:139], v[184:187], 0
	v_mfma_f32_16x16x32_bf16 v[44:47], v[132:135], v[164:167], v[44:47]
	v_mfma_f32_16x16x32_bf16 v[40:43], v[140:143], v[164:167], v[40:43]
	v_mfma_f32_16x16x32_bf16 v[28:31], v[132:135], v[172:175], v[28:31]
	v_mfma_f32_16x16x32_bf16 v[24:27], v[140:143], v[172:175], v[24:27]
	v_mfma_f32_16x16x32_bf16 v[12:15], v[132:135], v[180:183], v[12:15]
	v_mfma_f32_16x16x32_bf16 v[8:11], v[140:143], v[180:183], v[8:11]
	v_mfma_f32_16x16x32_bf16 v[4:7], v[132:135], v[188:191], v[4:7]
	v_mfma_f32_16x16x32_bf16 v[0:3], v[140:143], v[188:191], v[0:3]
	s_setprio 0
	s_barrier
	s_add_i32 s96, 0, 0x18000
	s_add_i32 s97, 0, 0x1c000
	v_add_u32_e32 v140, s96, v238
	v_add_u32_e32 v156, s97, v238
	ds_read_b128 v[128:131], v140
	ds_read_b128 v[132:135], v140 offset:1024
	ds_read_b128 v[136:139], v140 offset:2048
	ds_read_b128 v[140:143], v140 offset:3072
	ds_read_b128 v[144:147], v156
	ds_read_b128 v[148:151], v156 offset:1024
	ds_read_b128 v[152:155], v156 offset:2048
	ds_read_b128 v[156:159], v156 offset:3072
	s_mov_b32 m0, s82
	v_lshl_add_u64 v[224:225], s[12:13], 0, v[224:225]
	ds_read_b128 v[160:163], v240 offset:32768
	ds_read_b128 v[164:167], v240 offset:33792
	ds_read_b128 v[168:171], v240 offset:34816
	ds_read_b128 v[172:175], v240 offset:35840
	ds_read_b128 v[176:179], v240 offset:36864
	ds_read_b128 v[180:183], v240 offset:37888
	ds_read_b128 v[184:187], v240 offset:38912
	ds_read_b128 v[188:191], v240 offset:39936
	global_load_lds_dwordx4 v[224:225], off
	v_lshl_add_u64 v[222:223], s[12:13], 0, v[222:223]
	s_mov_b32 m0, s83
	s_nop 0
	global_load_lds_dwordx4 v[222:223], off
	s_waitcnt vmcnt(8)
	s_waitcnt lgkmcnt(0)
	s_barrier
	s_setprio 1
	s_waitcnt lgkmcnt(0)
	v_mfma_f32_16x16x32_bf16 v[124:127], v[128:131], v[160:163], v[124:127]
	v_mfma_f32_16x16x32_bf16 v[120:123], v[136:139], v[160:163], v[120:123]
	v_mfma_f32_16x16x32_bf16 v[116:119], v[128:131], v[168:171], v[116:119]
	v_mfma_f32_16x16x32_bf16 v[112:115], v[136:139], v[168:171], v[112:115]
	v_mfma_f32_16x16x32_bf16 v[100:103], v[128:131], v[176:179], v[100:103]
	v_mfma_f32_16x16x32_bf16 v[96:99], v[136:139], v[176:179], v[96:99]
	v_mfma_f32_16x16x32_bf16 v[84:87], v[128:131], v[184:187], v[84:87]
	v_mfma_f32_16x16x32_bf16 v[80:83], v[136:139], v[184:187], v[80:83]
	v_mfma_f32_16x16x32_bf16 v[124:127], v[132:135], v[164:167], v[124:127]
	v_mfma_f32_16x16x32_bf16 v[120:123], v[140:143], v[164:167], v[120:123]
	v_mfma_f32_16x16x32_bf16 v[116:119], v[132:135], v[172:175], v[116:119]
	v_mfma_f32_16x16x32_bf16 v[112:115], v[140:143], v[172:175], v[112:115]
	v_mfma_f32_16x16x32_bf16 v[100:103], v[132:135], v[180:183], v[100:103]
	v_mfma_f32_16x16x32_bf16 v[96:99], v[140:143], v[180:183], v[96:99]
	v_mfma_f32_16x16x32_bf16 v[84:87], v[132:135], v[188:191], v[84:87]
	v_mfma_f32_16x16x32_bf16 v[80:83], v[140:143], v[188:191], v[80:83]
	s_setprio 0
	s_setprio 1
	v_mfma_f32_16x16x32_bf16 v[108:111], v[144:147], v[160:163], v[108:111]
	v_mfma_f32_16x16x32_bf16 v[104:107], v[152:155], v[160:163], v[104:107]
	v_mfma_f32_16x16x32_bf16 v[92:95], v[144:147], v[168:171], v[92:95]
	v_mfma_f32_16x16x32_bf16 v[88:91], v[152:155], v[168:171], v[88:91]
	v_mfma_f32_16x16x32_bf16 v[76:79], v[144:147], v[176:179], v[76:79]
	v_mfma_f32_16x16x32_bf16 v[72:75], v[152:155], v[176:179], v[72:75]
	v_mfma_f32_16x16x32_bf16 v[68:71], v[144:147], v[184:187], v[68:71]
	v_mfma_f32_16x16x32_bf16 v[64:67], v[152:155], v[184:187], v[64:67]
	v_mfma_f32_16x16x32_bf16 v[108:111], v[148:151], v[164:167], v[108:111]
	v_mfma_f32_16x16x32_bf16 v[104:107], v[156:159], v[164:167], v[104:107]
	v_mfma_f32_16x16x32_bf16 v[92:95], v[148:151], v[172:175], v[92:95]
	v_mfma_f32_16x16x32_bf16 v[88:91], v[156:159], v[172:175], v[88:91]
	v_mfma_f32_16x16x32_bf16 v[76:79], v[148:151], v[180:183], v[76:79]
	v_mfma_f32_16x16x32_bf16 v[72:75], v[156:159], v[180:183], v[72:75]
	v_mfma_f32_16x16x32_bf16 v[68:71], v[148:151], v[188:191], v[68:71]
	v_mfma_f32_16x16x32_bf16 v[64:67], v[156:159], v[188:191], v[64:67]
	s_setprio 0
	s_barrier
; #define PG8_STAGE(bufoff, gbase, voff) do { _Pragma("unroll") for (int _i = 0; _i < 2; ++_i) \
;         __builtin_amdgcn_global_load_lds((const unsigned*)((const char*)(gbase) + (voff)[_i]), (LAS unsigned*)(lds + (bufoff) + ldsw + _i * 8192), 16, 0, 0); } while (0)
; #define PG8_LDA(dst, b, h) do { _Pragma("unroll") for (int m = 0; m < 4; ++m) _Pragma("unroll") for (int k = 0; k < 2; ++k) dst[m][k] = *(const LAS bf16x8*)(lds + PG8_SA(b, h) + aoff + m * 2048 + k * KOFF); } while (0)
; #define PG8_WAIT_V(n) asm volatile("s_waitcnt vmcnt(" #n ")" ::: "memory")
; #define PG8_WAIT_L(n) asm volatile("s_waitcnt lgkmcnt(" #n ")" ::: "memory")
; #define PG8_BAR __builtin_amdgcn_s_barrier()
; #define PG8_SCHED __builtin_amdgcn_sched_barrier(0)
; template <class Epi, class Sched, bool GATHER, bool FP8 = false, bool ALIGN = true>
; __device__ __forceinline__ void gemm_phase(LAS unsigned char* lds, int wave, const Gemm g, const Sched& S, const Epi& E) {
;     ...
;         for (int t = 0; t < nt; t += 2) {
;             const bool last = (t == nt - 2);
;             const char* a1 = Ab + (size_t)(t + 1) * kstep;
;             const char* a2 = last ? Ab : Ab + (size_t)(t + 2) * kstep; const char* b2 = last ? nB : cB + (size_t)(t + 2) * kstep;
;             const char* a3 = a2 + kstep; const char* b3 = b2 + kstep;
;     ...
;             PG8_LDA(At, 1, 1); PG8_STAGE(PG8_SB(1, 0), b3, voffB0); PG8_STAGE(PG8_SB(1, 1), b3, voffB1); PG8_STAGE(PG8_SA(1, 0), a3, ca0);
;             PG8_WAIT_V(8); PG8_WAIT_L(0); PG8_BAR; PG8_MMA(1, 0, At, B0); PG8_MMA(1, 1, At, B1); PG8_BAR; PG8_SCHED;
	s_add_i32 s12, s96, s22
	v_lshl_add_u64 v[196:197], v[196:197], 0, s[62:63]
	s_mov_b32 m0, s12
	ds_read_b128 v[160:163], v240 offset:49152
	ds_read_b128 v[164:167], v240 offset:50176
	ds_read_b128 v[168:171], v240 offset:51200
	ds_read_b128 v[172:175], v240 offset:52224
	ds_read_b128 v[176:179], v240 offset:53248
	ds_read_b128 v[180:183], v240 offset:54272
	ds_read_b128 v[184:187], v240 offset:55296
	ds_read_b128 v[188:191], v240 offset:56320
	global_load_lds_dwordx4 v[196:197], off
	v_lshl_add_u64 v[196:197], v[198:199], 0, s[62:63]
	s_add_i32 m0, s12, 0x2000
	s_add_i32 s12, s97, s22
	global_load_lds_dwordx4 v[196:197], off
	v_lshl_add_u64 v[196:197], v[200:201], 0, s[62:63]
	s_mov_b32 m0, s12
	s_nop 0
	global_load_lds_dwordx4 v[196:197], off
	v_lshl_add_u64 v[196:197], v[202:203], 0, s[62:63]
	s_add_i32 m0, s12, 0x2000
	s_nop 0
	global_load_lds_dwordx4 v[196:197], off
	v_lshl_add_u64 v[196:197], v[226:227], 0, s[62:63]
	s_mov_b32 m0, s86
	s_nop 0
	global_load_lds_dwordx4 v[196:197], off
	v_lshl_add_u64 v[196:197], v[228:229], 0, s[62:63]
	s_mov_b32 m0, s87
	s_nop 0
	global_load_lds_dwordx4 v[196:197], off
	s_waitcnt vmcnt(8)
	s_waitcnt lgkmcnt(0)
	s_barrier
	s_setprio 1
	s_waitcnt lgkmcnt(0)
	v_mfma_f32_16x16x32_bf16 v[60:63], v[128:131], v[160:163], v[60:63]
	v_mfma_f32_16x16x32_bf16 v[56:59], v[136:139], v[160:163], v[56:59]
	v_mfma_f32_16x16x32_bf16 v[52:55], v[128:131], v[168:171], v[52:55]
	v_mfma_f32_16x16x32_bf16 v[48:51], v[136:139], v[168:171], v[48:51]
	v_mfma_f32_16x16x32_bf16 v[36:39], v[128:131], v[176:179], v[36:39]
	v_mfma_f32_16x16x32_bf16 v[32:35], v[136:139], v[176:179], v[32:35]
	v_mfma_f32_16x16x32_bf16 v[20:23], v[128:131], v[184:187], v[20:23]
	v_mfma_f32_16x16x32_bf16 v[16:19], v[136:139], v[184:187], v[16:19]
	v_mfma_f32_16x16x32_bf16 v[60:63], v[132:135], v[164:167], v[60:63]
	v_mfma_f32_16x16x32_bf16 v[56:59], v[140:143], v[164:167], v[56:59]
	v_mfma_f32_16x16x32_bf16 v[52:55], v[132:135], v[172:175], v[52:55]
	v_mfma_f32_16x16x32_bf16 v[48:51], v[140:143], v[172:175], v[48:51]
	v_mfma_f32_16x16x32_bf16 v[36:39], v[132:135], v[180:183], v[36:39]
	v_mfma_f32_16x16x32_bf16 v[32:35], v[140:143], v[180:183], v[32:35]
	v_mfma_f32_16x16x32_bf16 v[20:23], v[132:135], v[188:191], v[20:23]
	v_mfma_f32_16x16x32_bf16 v[16:19], v[140:143], v[188:191], v[16:19]
	s_setprio 0
	s_setprio 1
	v_mfma_f32_16x16x32_bf16 v[44:47], v[144:147], v[160:163], v[44:47]
	v_mfma_f32_16x16x32_bf16 v[40:43], v[152:155], v[160:163], v[40:43]
	v_mfma_f32_16x16x32_bf16 v[28:31], v[144:147], v[168:171], v[28:31]
	v_mfma_f32_16x16x32_bf16 v[24:27], v[152:155], v[168:171], v[24:27]
	v_mfma_f32_16x16x32_bf16 v[12:15], v[144:147], v[176:179], v[12:15]
	v_mfma_f32_16x16x32_bf16 v[8:11], v[152:155], v[176:179], v[8:11]
	v_mfma_f32_16x16x32_bf16 v[4:7], v[144:147], v[184:187], v[4:7]
	v_mfma_f32_16x16x32_bf16 v[0:3], v[152:155], v[184:187], v[0:3]
	v_mfma_f32_16x16x32_bf16 v[44:47], v[148:151], v[164:167], v[44:47]
	v_mfma_f32_16x16x32_bf16 v[40:43], v[156:159], v[164:167], v[40:43]
	v_mfma_f32_16x16x32_bf16 v[28:31], v[148:151], v[172:175], v[28:31]
	v_mfma_f32_16x16x32_bf16 v[24:27], v[156:159], v[172:175], v[24:27]
	v_mfma_f32_16x16x32_bf16 v[12:15], v[148:151], v[180:183], v[12:15]
	v_mfma_f32_16x16x32_bf16 v[8:11], v[156:159], v[180:183], v[8:11]
	v_mfma_f32_16x16x32_bf16 v[4:7], v[148:151], v[188:191], v[4:7]
	v_mfma_f32_16x16x32_bf16 v[0:3], v[156:159], v[188:191], v[0:3]
	s_setprio 0
	s_barrier
	s_add_i32 s95, s95, 2
	s_add_u32 s80, s80, 0x100
	s_addc_u32 s81, s81, 0
	s_add_u32 s93, s93, 0x100
	s_addc_u32 s94, s94, 0
	s_cmp_gt_u32 s95, 29
	s_cbranch_scc1 .LBB0_259
	s_branch .LBB0_257

; #define PG8_STAGE(bufoff, gbase, voff) do { _Pragma("unroll") for (int _i = 0; _i < 2; ++_i) \
;         __builtin_amdgcn_global_load_lds((const unsigned*)((const char*)(gbase) + (voff)[_i]), (LAS unsigned*)(lds + (bufoff) + ldsw + _i * 8192), 16, 0, 0); } while (0)
; #define PG8_LDA(dst, b, h) do { _Pragma("unroll") for (int m = 0; m < 4; ++m) _Pragma("unroll") for (int k = 0; k < 2; ++k) dst[m][k] = *(const LAS bf16x8*)(lds + PG8_SA(b, h) + aoff + m * 2048 + k * KOFF); } while (0)
; #define PG8_LDB(dst, b, h) do { _Pragma("unroll") for (int n = 0; n < 2; ++n) _Pragma("unroll") for (int k = 0; k < 2; ++k) dst[n][k] = *(const LAS bf16x8*)(lds + PG8_SB(b, h) + boff + n * 2048 + k * KOFF); } while (0)
; #define PG8_WAIT_V(n) asm volatile("s_waitcnt vmcnt(" #n ")" ::: "memory")
; #define PG8_WAIT_L(n) asm volatile("s_waitcnt lgkmcnt(" #n ")" ::: "memory")
; template <class Epi, class Sched, bool GATHER, bool FP8 = false, bool ALIGN = true>
; __device__ __forceinline__ void gemm_phase(LAS unsigned char* lds, int wave, const Gemm g, const Sched& S, const Epi& E) {
;     ...
;         const bool has_next = S.next(ui + 1, nxt);
;         const char* nB = has_next ? (const char*)g.Bt + (size_t)nxt.e * g.b_estride + (size_t)nxt.pn * tstep : cB;
; #pragma unroll 1
;         for (int t = 0; t < nt; t += 2) {
;             const bool last = (t == nt - 2);
;             const char* a1 = Ab + (size_t)(t + 1) * kstep;
;             const char* a2 = last ? Ab : Ab + (size_t)(t + 2) * kstep; const char* b2 = last ? nB : cB + (size_t)(t + 2) * kstep;
;             const char* a3 = a2 + kstep; const char* b3 = b2 + kstep;
;             PG8_LDB(B0, 0, 0); PG8_LDB(B1, 0, 1); PG8_SCHED; PG8_LDA(At, 0, 0); PG8_STAGE(PG8_SA(1, 1), a1, ca1);
;             if (last && has_next) PG8_AOFF(nxt, ca0, ca1);
;             PG8_WAIT_V(8); PG8_WAIT_L(0); PG8_BAR; PG8_MMA(0, 0, At, B0); PG8_MMA(0, 1, At, B1); PG8_BAR; PG8_SCHED;
;             PG8_LDA(At, 0, 1); PG8_STAGE(PG8_SB(0, 0), b2, voffB0); PG8_STAGE(PG8_SB(0, 1), b2, voffB1); PG8_STAGE(PG8_SA(0, 0), a2, ca0);
;     ...
;         for (int a = 0; a < 2; ++a)
; #pragma unroll
;             for (int b = 0; b < 2; ++b)
; #pragma unroll
;                 for (int m = 0; m < 4; ++m)
; #pragma unroll
;                     for (int n = 0; n < 2; ++n) acc[a][b][m][n] = (f32x4){0.f, 0.f, 0.f, 0.f};
;         cur = nxt; cB = nB; ++ui;
.LBB0_274:
	s_ashr_i32 s11, s10, 31
	s_lshl_b64 s[12:13], s[10:11], 20
	s_add_u32 s44, s34, s12
	s_addc_u32 s45, s35, s13
	s_and_b64 s[12:13], s[40:41], exec
	s_cselect_b32 s11, s45, s47
	s_cselect_b32 s31, s44, s46
	s_lshl_b32 s12, s24, 20
	v_add_u32_e32 v241, s12, v235
	v_add_u32_e32 v242, s12, v236
	s_add_u32 s80, s46, 0x100
	v_add_u32_e32 v218, 0x80000, v241
	v_add_u32_e32 v220, 0x80000, v242
	v_mov_b32_e32 v219, v193
	v_mov_b32_e32 v221, v193
	s_addc_u32 s81, s47, 0
	s_mov_b32 s82, -2
	s_mov_b64 s[46:47], s[6:7]
.Lpeel_p0q_h:
	v_add_u32_e32 v128, 0, v238
	v_add_u32_e32 v129, 0x10000, v128
	v_add_u32_e32 v140, 0x14000, v128
	ds_read_b128 v[144:147], v129
	ds_read_b128 v[148:151], v129 offset:1024
	ds_read_b128 v[152:155], v129 offset:2048
	ds_read_b128 v[156:159], v129 offset:3072
	ds_read_b128 v[128:131], v140
	ds_read_b128 v[132:135], v140 offset:1024
	ds_read_b128 v[136:139], v140 offset:2048
	ds_read_b128 v[140:143], v140 offset:3072
	s_cmp_eq_u32 s82, 28
	s_cselect_b64 s[12:13], -1, 0
	s_add_i32 m0, s49, 0xc000
	ds_read_b128 v[184:187], v240
	ds_read_b128 v[188:191], v240 offset:1024
	ds_read_b128 v[176:179], v240 offset:2048
	ds_read_b128 v[180:183], v240 offset:3072
	ds_read_b128 v[168:171], v240 offset:4096
	ds_read_b128 v[172:175], v240 offset:5120
	ds_read_b128 v[160:163], v240 offset:6144
	ds_read_b128 v[164:167], v240 offset:7168
	global_load_lds_dwordx4 v214, s[46:47]
	s_add_i32 m0, s49, 0xe000
	s_and_b64 s[84:85], s[40:41], s[12:13]
	global_load_lds_dwordx4 v216, s[46:47]
	s_andn2_b64 vcc, exec, s[84:85]
	s_cbranch_vccz .Lpeel_p0q_a
	v_mov_b32_e32 v215, v193
	v_mov_b32_e32 v217, v193
	v_mov_b64_e32 v[222:223], v[216:217]
	v_mov_b64_e32 v[224:225], v[214:215]
	s_branch .Lpeel_p0q_b
.Lpeel_p0q_a:
	v_mov_b64_e32 v[222:223], v[220:221]
	v_mov_b64_e32 v[224:225], v[218:219]
	v_mov_b32_e32 v212, v242
	v_mov_b32_e32 v192, v241
	v_mov_b32_e32 v216, v220
	v_mov_b32_e32 v214, v218
.Lpeel_p0q_b:
	s_waitcnt vmcnt(8)
	s_add_u32 s83, s46, 0x80
	s_waitcnt lgkmcnt(0)
	s_addc_u32 s84, s47, 0
	s_and_b64 s[12:13], s[12:13], exec
	s_cselect_b32 s13, s5, s84
	s_cselect_b32 s12, s4, s83
	s_cselect_b32 s85, s11, s81
	s_cselect_b32 s84, s31, s80
	s_barrier
	s_setprio 1
	s_waitcnt lgkmcnt(0)
	v_mfma_f32_16x16x32_bf16 v[124:127], v[144:147], v[184:187], 0
	v_mfma_f32_16x16x32_bf16 v[120:123], v[152:155], v[184:187], 0
	v_mfma_f32_16x16x32_bf16 v[116:119], v[144:147], v[176:179], 0
	v_mfma_f32_16x16x32_bf16 v[112:115], v[152:155], v[176:179], 0
	v_mfma_f32_16x16x32_bf16 v[100:103], v[144:147], v[168:171], 0
	v_mfma_f32_16x16x32_bf16 v[96:99], v[152:155], v[168:171], 0
	v_mfma_f32_16x16x32_bf16 v[84:87], v[144:147], v[160:163], 0
	v_mfma_f32_16x16x32_bf16 v[80:83], v[152:155], v[160:163], 0
	v_mfma_f32_16x16x32_bf16 v[124:127], v[148:151], v[188:191], v[124:127]
	v_mfma_f32_16x16x32_bf16 v[120:123], v[156:159], v[188:191], v[120:123]
	v_mfma_f32_16x16x32_bf16 v[116:119], v[148:151], v[180:183], v[116:119]
	v_mfma_f32_16x16x32_bf16 v[112:115], v[156:159], v[180:183], v[112:115]
	v_mfma_f32_16x16x32_bf16 v[100:103], v[148:151], v[172:175], v[100:103]
	v_mfma_f32_16x16x32_bf16 v[96:99], v[156:159], v[172:175], v[96:99]
	v_mfma_f32_16x16x32_bf16 v[84:87], v[148:151], v[164:167], v[84:87]
	v_mfma_f32_16x16x32_bf16 v[80:83], v[156:159], v[164:167], v[80:83]
	s_setprio 0
	s_setprio 1
	v_mfma_f32_16x16x32_bf16 v[108:111], v[128:131], v[184:187], 0
	v_mfma_f32_16x16x32_bf16 v[104:107], v[136:139], v[184:187], 0
	v_mfma_f32_16x16x32_bf16 v[92:95], v[128:131], v[176:179], 0
	v_mfma_f32_16x16x32_bf16 v[88:91], v[136:139], v[176:179], 0
	v_mfma_f32_16x16x32_bf16 v[76:79], v[128:131], v[168:171], 0
	v_mfma_f32_16x16x32_bf16 v[72:75], v[136:139], v[168:171], 0
	v_mfma_f32_16x16x32_bf16 v[68:71], v[128:131], v[160:163], 0
	v_mfma_f32_16x16x32_bf16 v[64:67], v[136:139], v[160:163], 0
	v_mfma_f32_16x16x32_bf16 v[108:111], v[132:135], v[188:191], v[108:111]
	v_mfma_f32_16x16x32_bf16 v[104:107], v[140:143], v[188:191], v[104:107]
	v_mfma_f32_16x16x32_bf16 v[92:95], v[132:135], v[180:183], v[92:95]
	v_mfma_f32_16x16x32_bf16 v[88:91], v[140:143], v[180:183], v[88:91]
	v_mfma_f32_16x16x32_bf16 v[76:79], v[132:135], v[172:175], v[76:79]
	v_mfma_f32_16x16x32_bf16 v[72:75], v[140:143], v[172:175], v[72:75]
	v_mfma_f32_16x16x32_bf16 v[68:71], v[132:135], v[164:167], v[68:71]
	v_mfma_f32_16x16x32_bf16 v[64:67], v[140:143], v[164:167], v[64:67]
	s_setprio 0
	s_barrier
	s_mov_b32 m0, s50
	v_lshl_add_u64 v[196:197], s[84:85], 0, v[208:209]
	ds_read_b128 v[160:163], v240 offset:16384
	ds_read_b128 v[164:167], v240 offset:17408
	ds_read_b128 v[168:171], v240 offset:18432
	ds_read_b128 v[172:175], v240 offset:19456
	ds_read_b128 v[176:179], v240 offset:20480
	ds_read_b128 v[180:183], v240 offset:21504
	ds_read_b128 v[184:187], v240 offset:22528
	ds_read_b128 v[188:191], v240 offset:23552
	global_load_lds_dwordx4 v[196:197], off
	v_lshl_add_u64 v[198:199], s[84:85], 0, v[204:205]
	s_mov_b32 m0, s51
	v_lshl_add_u64 v[200:201], s[84:85], 0, v[210:211]
	global_load_lds_dwordx4 v[198:199], off
	s_mov_b32 m0, s53
	v_lshl_add_u64 v[202:203], s[84:85], 0, v[206:207]
	global_load_lds_dwordx4 v[200:201], off
	s_mov_b32 m0, s56
	v_mov_b32_e32 v213, v193
	global_load_lds_dwordx4 v[202:203], off
	s_mov_b32 m0, s49
	v_lshl_add_u64 v[226:227], s[12:13], 0, v[192:193]
	global_load_lds_dwordx4 v192, s[12:13]
	s_mov_b32 m0, s57
	v_lshl_add_u64 v[228:229], s[12:13], 0, v[212:213]
	global_load_lds_dwordx4 v212, s[12:13]
	s_waitcnt vmcnt(8)
	s_waitcnt lgkmcnt(0)
	s_barrier
; #define PG8_STAGE(bufoff, gbase, voff) do { _Pragma("unroll") for (int _i = 0; _i < 2; ++_i) \
;         __builtin_amdgcn_global_load_lds((const unsigned*)((const char*)(gbase) + (voff)[_i]), (LAS unsigned*)(lds + (bufoff) + ldsw + _i * 8192), 16, 0, 0); } while (0)
; #define PG8_LDA(dst, b, h) do { _Pragma("unroll") for (int m = 0; m < 4; ++m) _Pragma("unroll") for (int k = 0; k < 2; ++k) dst[m][k] = *(const LAS bf16x8*)(lds + PG8_SA(b, h) + aoff + m * 2048 + k * KOFF); } while (0)
; #define PG8_LDB(dst, b, h) do { _Pragma("unroll") for (int n = 0; n < 2; ++n) _Pragma("unroll") for (int k = 0; k < 2; ++k) dst[n][k] = *(const LAS bf16x8*)(lds + PG8_SB(b, h) + boff + n * 2048 + k * KOFF); } while (0)
; #define PG8_WAIT_V(n) asm volatile("s_waitcnt vmcnt(" #n ")" ::: "memory")
; #define PG8_WAIT_L(n) asm volatile("s_waitcnt lgkmcnt(" #n ")" ::: "memory")
; #define PG8_BAR __builtin_amdgcn_s_barrier()
; #define PG8_SCHED __builtin_amdgcn_sched_barrier(0)
; template <class Epi, class Sched, bool GATHER, bool FP8 = false, bool ALIGN = true>
; __device__ __forceinline__ void gemm_phase(LAS unsigned char* lds, int wave, const Gemm g, const Sched& S, const Epi& E) {
;     ...
;             PG8_WAIT_V(8); PG8_WAIT_L(0); PG8_BAR; PG8_MMA(1, 0, At, B0); PG8_MMA(1, 1, At, B1); PG8_BAR; PG8_SCHED;
;             PG8_LDB(B0, 1, 0); PG8_LDB(B1, 1, 1); PG8_SCHED; PG8_LDA(At, 1, 0); PG8_STAGE(PG8_SA(0, 1), a2, ca1);
;             PG8_WAIT_V(8); PG8_WAIT_L(0); PG8_BAR; PG8_MMA(0, 0, At, B0); PG8_MMA(0, 1, At, B1); PG8_BAR; PG8_SCHED;
	s_setprio 1
	s_waitcnt lgkmcnt(0)
	v_mfma_f32_16x16x32_bf16 v[60:63], v[144:147], v[160:163], 0
	v_mfma_f32_16x16x32_bf16 v[56:59], v[152:155], v[160:163], 0
	v_mfma_f32_16x16x32_bf16 v[52:55], v[144:147], v[168:171], 0
	v_mfma_f32_16x16x32_bf16 v[48:51], v[152:155], v[168:171], 0
	v_mfma_f32_16x16x32_bf16 v[36:39], v[144:147], v[176:179], 0
	v_mfma_f32_16x16x32_bf16 v[32:35], v[152:155], v[176:179], 0
	v_mfma_f32_16x16x32_bf16 v[20:23], v[144:147], v[184:187], 0
	v_mfma_f32_16x16x32_bf16 v[16:19], v[152:155], v[184:187], 0
	v_mfma_f32_16x16x32_bf16 v[60:63], v[148:151], v[164:167], v[60:63]
	v_mfma_f32_16x16x32_bf16 v[56:59], v[156:159], v[164:167], v[56:59]
	v_mfma_f32_16x16x32_bf16 v[52:55], v[148:151], v[172:175], v[52:55]
	v_mfma_f32_16x16x32_bf16 v[48:51], v[156:159], v[172:175], v[48:51]
	v_mfma_f32_16x16x32_bf16 v[36:39], v[148:151], v[180:183], v[36:39]
	v_mfma_f32_16x16x32_bf16 v[32:35], v[156:159], v[180:183], v[32:35]
	v_mfma_f32_16x16x32_bf16 v[20:23], v[148:151], v[188:191], v[20:23]
	v_mfma_f32_16x16x32_bf16 v[16:19], v[156:159], v[188:191], v[16:19]
	s_setprio 0
	s_setprio 1
	v_mfma_f32_16x16x32_bf16 v[44:47], v[128:131], v[160:163], 0
	v_mfma_f32_16x16x32_bf16 v[40:43], v[136:139], v[160:163], 0
	v_mfma_f32_16x16x32_bf16 v[28:31], v[128:131], v[168:171], 0
	v_mfma_f32_16x16x32_bf16 v[24:27], v[136:139], v[168:171], 0
	v_mfma_f32_16x16x32_bf16 v[12:15], v[128:131], v[176:179], 0
	v_mfma_f32_16x16x32_bf16 v[8:11], v[136:139], v[176:179], 0
	v_mfma_f32_16x16x32_bf16 v[4:7], v[128:131], v[184:187], 0
	v_mfma_f32_16x16x32_bf16 v[0:3], v[136:139], v[184:187], 0
	v_mfma_f32_16x16x32_bf16 v[44:47], v[132:135], v[164:167], v[44:47]
	v_mfma_f32_16x16x32_bf16 v[40:43], v[140:143], v[164:167], v[40:43]
	v_mfma_f32_16x16x32_bf16 v[28:31], v[132:135], v[172:175], v[28:31]
	v_mfma_f32_16x16x32_bf16 v[24:27], v[140:143], v[172:175], v[24:27]
	v_mfma_f32_16x16x32_bf16 v[12:15], v[132:135], v[180:183], v[12:15]
	v_mfma_f32_16x16x32_bf16 v[8:11], v[140:143], v[180:183], v[8:11]
	v_mfma_f32_16x16x32_bf16 v[4:7], v[132:135], v[188:191], v[4:7]
	v_mfma_f32_16x16x32_bf16 v[0:3], v[140:143], v[188:191], v[0:3]
	s_setprio 0
	s_barrier
	s_add_i32 s83, 0, 0x18000
	s_add_i32 s84, 0, 0x1c000
	v_add_u32_e32 v140, s83, v238
	v_add_u32_e32 v156, s84, v238
	ds_read_b128 v[128:131], v140
	ds_read_b128 v[132:135], v140 offset:1024
	ds_read_b128 v[136:139], v140 offset:2048
	ds_read_b128 v[140:143], v140 offset:3072
	ds_read_b128 v[144:147], v156
	ds_read_b128 v[148:151], v156 offset:1024
	ds_read_b128 v[152:155], v156 offset:2048
	ds_read_b128 v[156:159], v156 offset:3072
	s_mov_b32 m0, s58
	v_lshl_add_u64 v[224:225], s[12:13], 0, v[224:225]
	ds_read_b128 v[160:163], v240 offset:32768
	ds_read_b128 v[164:167], v240 offset:33792
	ds_read_b128 v[168:171], v240 offset:34816
	ds_read_b128 v[172:175], v240 offset:35840
	ds_read_b128 v[176:179], v240 offset:36864
	ds_read_b128 v[180:183], v240 offset:37888
	ds_read_b128 v[184:187], v240 offset:38912
	ds_read_b128 v[188:191], v240 offset:39936
	global_load_lds_dwordx4 v[224:225], off
	v_lshl_add_u64 v[222:223], s[12:13], 0, v[222:223]
	s_mov_b32 m0, s59
	s_nop 0
	global_load_lds_dwordx4 v[222:223], off
	s_waitcnt vmcnt(8)
	s_waitcnt lgkmcnt(0)
	s_barrier
	s_setprio 1
	s_waitcnt lgkmcnt(0)
	v_mfma_f32_16x16x32_bf16 v[124:127], v[128:131], v[160:163], v[124:127]
	v_mfma_f32_16x16x32_bf16 v[120:123], v[136:139], v[160:163], v[120:123]
	v_mfma_f32_16x16x32_bf16 v[116:119], v[128:131], v[168:171], v[116:119]
	v_mfma_f32_16x16x32_bf16 v[112:115], v[136:139], v[168:171], v[112:115]
	v_mfma_f32_16x16x32_bf16 v[100:103], v[128:131], v[176:179], v[100:103]
	v_mfma_f32_16x16x32_bf16 v[96:99], v[136:139], v[176:179], v[96:99]
	v_mfma_f32_16x16x32_bf16 v[84:87], v[128:131], v[184:187], v[84:87]
	v_mfma_f32_16x16x32_bf16 v[80:83], v[136:139], v[184:187], v[80:83]
	v_mfma_f32_16x16x32_bf16 v[124:127], v[132:135], v[164:167], v[124:127]
	v_mfma_f32_16x16x32_bf16 v[120:123], v[140:143], v[164:167], v[120:123]
	v_mfma_f32_16x16x32_bf16 v[116:119], v[132:135], v[172:175], v[116:119]
	v_mfma_f32_16x16x32_bf16 v[112:115], v[140:143], v[172:175], v[112:115]
	v_mfma_f32_16x16x32_bf16 v[100:103], v[132:135], v[180:183], v[100:103]
	v_mfma_f32_16x16x32_bf16 v[96:99], v[140:143], v[180:183], v[96:99]
	v_mfma_f32_16x16x32_bf16 v[84:87], v[132:135], v[188:191], v[84:87]
	v_mfma_f32_16x16x32_bf16 v[80:83], v[140:143], v[188:191], v[80:83]
	s_setprio 0
	s_setprio 1
	v_mfma_f32_16x16x32_bf16 v[108:111], v[144:147], v[160:163], v[108:111]
	v_mfma_f32_16x16x32_bf16 v[104:107], v[152:155], v[160:163], v[104:107]
	v_mfma_f32_16x16x32_bf16 v[92:95], v[144:147], v[168:171], v[92:95]
	v_mfma_f32_16x16x32_bf16 v[88:91], v[152:155], v[168:171], v[88:91]
	v_mfma_f32_16x16x32_bf16 v[76:79], v[144:147], v[176:179], v[76:79]
	v_mfma_f32_16x16x32_bf16 v[72:75], v[152:155], v[176:179], v[72:75]
	v_mfma_f32_16x16x32_bf16 v[68:71], v[144:147], v[184:187], v[68:71]
	v_mfma_f32_16x16x32_bf16 v[64:67], v[152:155], v[184:187], v[64:67]
	v_mfma_f32_16x16x32_bf16 v[108:111], v[148:151], v[164:167], v[108:111]
	v_mfma_f32_16x16x32_bf16 v[104:107], v[156:159], v[164:167], v[104:107]
	v_mfma_f32_16x16x32_bf16 v[92:95], v[148:151], v[172:175], v[92:95]
	v_mfma_f32_16x16x32_bf16 v[88:91], v[156:159], v[172:175], v[88:91]
	v_mfma_f32_16x16x32_bf16 v[76:79], v[148:151], v[180:183], v[76:79]
	v_mfma_f32_16x16x32_bf16 v[72:75], v[156:159], v[180:183], v[72:75]
	v_mfma_f32_16x16x32_bf16 v[68:71], v[148:151], v[188:191], v[68:71]
	v_mfma_f32_16x16x32_bf16 v[64:67], v[156:159], v[188:191], v[64:67]
	s_setprio 0
	s_barrier
; #define PG8_STAGE(bufoff, gbase, voff) do { _Pragma("unroll") for (int _i = 0; _i < 2; ++_i) \
;         __builtin_amdgcn_global_load_lds((const unsigned*)((const char*)(gbase) + (voff)[_i]), (LAS unsigned*)(lds + (bufoff) + ldsw + _i * 8192), 16, 0, 0); } while (0)
; #define PG8_LDA(dst, b, h) do { _Pragma("unroll") for (int m = 0; m < 4; ++m) _Pragma("unroll") for (int k = 0; k < 2; ++k) dst[m][k] = *(const LAS bf16x8*)(lds + PG8_SA(b, h) + aoff + m * 2048 + k * KOFF); } while (0)
; #define PG8_WAIT_V(n) asm volatile("s_waitcnt vmcnt(" #n ")" ::: "memory")
; #define PG8_WAIT_L(n) asm volatile("s_waitcnt lgkmcnt(" #n ")" ::: "memory")
; #define PG8_BAR __builtin_amdgcn_s_barrier()
; #define PG8_SCHED __builtin_amdgcn_sched_barrier(0)
; template <class Epi, class Sched, bool GATHER, bool FP8 = false, bool ALIGN = true>
; __device__ __forceinline__ void gemm_phase(LAS unsigned char* lds, int wave, const Gemm g, const Sched& S, const Epi& E) {
;     ...
;         for (int t = 0; t < nt; t += 2) {
;             const bool last = (t == nt - 2);
;             const char* a1 = Ab + (size_t)(t + 1) * kstep;
;             const char* a2 = last ? Ab : Ab + (size_t)(t + 2) * kstep; const char* b2 = last ? nB : cB + (size_t)(t + 2) * kstep;
;             const char* a3 = a2 + kstep; const char* b3 = b2 + kstep;
;     ...
;             PG8_LDA(At, 1, 1); PG8_STAGE(PG8_SB(1, 0), b3, voffB0); PG8_STAGE(PG8_SB(1, 1), b3, voffB1); PG8_STAGE(PG8_SA(1, 0), a3, ca0);
;             PG8_WAIT_V(8); PG8_WAIT_L(0); PG8_BAR; PG8_MMA(1, 0, At, B0); PG8_MMA(1, 1, At, B1); PG8_BAR; PG8_SCHED;
	s_add_i32 s12, s83, s22
	v_lshl_add_u64 v[196:197], v[196:197], 0, s[62:63]
	s_mov_b32 m0, s12
	ds_read_b128 v[160:163], v240 offset:49152
	ds_read_b128 v[164:167], v240 offset:50176
	ds_read_b128 v[168:171], v240 offset:51200
	ds_read_b128 v[172:175], v240 offset:52224
	ds_read_b128 v[176:179], v240 offset:53248
	ds_read_b128 v[180:183], v240 offset:54272
	ds_read_b128 v[184:187], v240 offset:55296
	ds_read_b128 v[188:191], v240 offset:56320
	global_load_lds_dwordx4 v[196:197], off
	v_lshl_add_u64 v[196:197], v[198:199], 0, s[62:63]
	s_add_i32 m0, s12, 0x2000
	s_add_i32 s12, s84, s22
	global_load_lds_dwordx4 v[196:197], off
	v_lshl_add_u64 v[196:197], v[200:201], 0, s[62:63]
	s_mov_b32 m0, s12
	s_nop 0
	global_load_lds_dwordx4 v[196:197], off
	v_lshl_add_u64 v[196:197], v[202:203], 0, s[62:63]
	s_add_i32 m0, s12, 0x2000
	s_nop 0
	global_load_lds_dwordx4 v[196:197], off
	v_lshl_add_u64 v[196:197], v[226:227], 0, s[62:63]
	s_mov_b32 m0, s29
	s_nop 0
	global_load_lds_dwordx4 v[196:197], off
	v_lshl_add_u64 v[196:197], v[228:229], 0, s[62:63]
	s_mov_b32 m0, s30
	s_nop 0
	global_load_lds_dwordx4 v[196:197], off
	s_waitcnt vmcnt(8)
	s_waitcnt lgkmcnt(0)
	s_barrier
	s_setprio 1
	s_waitcnt lgkmcnt(0)
	v_mfma_f32_16x16x32_bf16 v[60:63], v[128:131], v[160:163], v[60:63]
	v_mfma_f32_16x16x32_bf16 v[56:59], v[136:139], v[160:163], v[56:59]
	v_mfma_f32_16x16x32_bf16 v[52:55], v[128:131], v[168:171], v[52:55]
	v_mfma_f32_16x16x32_bf16 v[48:51], v[136:139], v[168:171], v[48:51]
	v_mfma_f32_16x16x32_bf16 v[36:39], v[128:131], v[176:179], v[36:39]
	v_mfma_f32_16x16x32_bf16 v[32:35], v[136:139], v[176:179], v[32:35]
	v_mfma_f32_16x16x32_bf16 v[20:23], v[128:131], v[184:187], v[20:23]
	v_mfma_f32_16x16x32_bf16 v[16:19], v[136:139], v[184:187], v[16:19]
	v_mfma_f32_16x16x32_bf16 v[60:63], v[132:135], v[164:167], v[60:63]
	v_mfma_f32_16x16x32_bf16 v[56:59], v[140:143], v[164:167], v[56:59]
	v_mfma_f32_16x16x32_bf16 v[52:55], v[132:135], v[172:175], v[52:55]
	v_mfma_f32_16x16x32_bf16 v[48:51], v[140:143], v[172:175], v[48:51]
	v_mfma_f32_16x16x32_bf16 v[36:39], v[132:135], v[180:183], v[36:39]
	v_mfma_f32_16x16x32_bf16 v[32:35], v[140:143], v[180:183], v[32:35]
	v_mfma_f32_16x16x32_bf16 v[20:23], v[132:135], v[188:191], v[20:23]
	v_mfma_f32_16x16x32_bf16 v[16:19], v[140:143], v[188:191], v[16:19]
	s_setprio 0
	s_setprio 1
	v_mfma_f32_16x16x32_bf16 v[44:47], v[144:147], v[160:163], v[44:47]
	v_mfma_f32_16x16x32_bf16 v[40:43], v[152:155], v[160:163], v[40:43]
	v_mfma_f32_16x16x32_bf16 v[28:31], v[144:147], v[168:171], v[28:31]
	v_mfma_f32_16x16x32_bf16 v[24:27], v[152:155], v[168:171], v[24:27]
	v_mfma_f32_16x16x32_bf16 v[12:15], v[144:147], v[176:179], v[12:15]
	v_mfma_f32_16x16x32_bf16 v[8:11], v[152:155], v[176:179], v[8:11]
	v_mfma_f32_16x16x32_bf16 v[4:7], v[144:147], v[184:187], v[4:7]
	v_mfma_f32_16x16x32_bf16 v[0:3], v[152:155], v[184:187], v[0:3]
	v_mfma_f32_16x16x32_bf16 v[44:47], v[148:151], v[164:167], v[44:47]
	v_mfma_f32_16x16x32_bf16 v[40:43], v[156:159], v[164:167], v[40:43]
	v_mfma_f32_16x16x32_bf16 v[28:31], v[148:151], v[172:175], v[28:31]
	v_mfma_f32_16x16x32_bf16 v[24:27], v[156:159], v[172:175], v[24:27]
	v_mfma_f32_16x16x32_bf16 v[12:15], v[148:151], v[180:183], v[12:15]
	v_mfma_f32_16x16x32_bf16 v[8:11], v[156:159], v[180:183], v[8:11]
	v_mfma_f32_16x16x32_bf16 v[4:7], v[148:151], v[188:191], v[4:7]
	v_mfma_f32_16x16x32_bf16 v[0:3], v[156:159], v[188:191], v[0:3]
	s_setprio 0
	s_barrier
	s_add_i32 s82, s82, 2
	s_add_u32 s46, s46, 0x100
	s_addc_u32 s47, s47, 0
	s_add_u32 s80, s80, 0x100
	s_addc_u32 s81, s81, 0
	s_cmp_gt_u32 s82, 29
	s_cbranch_scc1 .LBB0_279
	s_branch .LBB0_277

; #define PG8_STAGE(bufoff, gbase, voff) do { _Pragma("unroll") for (int _i = 0; _i < 2; ++_i) \
;         __builtin_amdgcn_global_load_lds((const unsigned*)((const char*)(gbase) + (voff)[_i]), (LAS unsigned*)(lds + (bufoff) + ldsw + _i * 8192), 16, 0, 0); } while (0)
; #define PG8_LDA(dst, b, h) do { _Pragma("unroll") for (int m = 0; m < 4; ++m) _Pragma("unroll") for (int k = 0; k < 2; ++k) dst[m][k] = *(const LAS bf16x8*)(lds + PG8_SA(b, h) + aoff + m * 2048 + k * KOFF); } while (0)
; #define PG8_LDB(dst, b, h) do { _Pragma("unroll") for (int n = 0; n < 2; ++n) _Pragma("unroll") for (int k = 0; k < 2; ++k) dst[n][k] = *(const LAS bf16x8*)(lds + PG8_SB(b, h) + boff + n * 2048 + k * KOFF); } while (0)
; #define PG8_WAIT_V(n) asm volatile("s_waitcnt vmcnt(" #n ")" ::: "memory")
; #define PG8_WAIT_L(n) asm volatile("s_waitcnt lgkmcnt(" #n ")" ::: "memory")
; template <class Epi, class Sched, bool GATHER, bool FP8 = false, bool ALIGN = true>
; __device__ __forceinline__ void gemm_phase(LAS unsigned char* lds, int wave, const Gemm g, const Sched& S, const Epi& E) {
;     ...
;         const bool has_next = S.next(ui + 1, nxt);
;         const char* nB = has_next ? (const char*)g.Bt + (size_t)nxt.e * g.b_estride + (size_t)nxt.pn * tstep : cB;
; #pragma unroll 1
;         for (int t = 0; t < nt; t += 2) {
;             const bool last = (t == nt - 2);
;             const char* a1 = Ab + (size_t)(t + 1) * kstep;
;             const char* a2 = last ? Ab : Ab + (size_t)(t + 2) * kstep; const char* b2 = last ? nB : cB + (size_t)(t + 2) * kstep;
;             const char* a3 = a2 + kstep; const char* b3 = b2 + kstep;
;             PG8_LDB(B0, 0, 0); PG8_LDB(B1, 0, 1); PG8_SCHED; PG8_LDA(At, 0, 0); PG8_STAGE(PG8_SA(1, 1), a1, ca1);
;             if (last && has_next) PG8_AOFF(nxt, ca0, ca1);
;             PG8_WAIT_V(8); PG8_WAIT_L(0); PG8_BAR; PG8_MMA(0, 0, At, B0); PG8_MMA(0, 1, At, B1); PG8_BAR; PG8_SCHED;
;             PG8_LDA(At, 0, 1); PG8_STAGE(PG8_SB(0, 0), b2, voffB0); PG8_STAGE(PG8_SB(0, 1), b2, voffB1); PG8_STAGE(PG8_SA(0, 0), a2, ca0);
;     ...
;         for (int a = 0; a < 2; ++a)
; #pragma unroll
;             for (int b = 0; b < 2; ++b)
; #pragma unroll
;                 for (int m = 0; m < 4; ++m)
; #pragma unroll
;                     for (int n = 0; n < 2; ++n) acc[a][b][m][n] = (f32x4){0.f, 0.f, 0.f, 0.f};
;         cur = nxt; cB = nB; ++ui;
.LBB0_404:
	s_ashr_i32 s47, s46, 31
	s_lshl_b64 s[12:13], s[46:47], 20
	s_add_u32 s48, s22, s12
	s_addc_u32 s49, s24, s13
	s_and_b64 s[12:13], s[38:39], exec
	s_cselect_b32 s47, s49, s51
	s_cselect_b32 s85, s48, s50
	s_lshl_b32 s12, s84, 20
	v_add_u32_e32 v241, s12, v235
	v_add_u32_e32 v242, s12, v236
	s_add_u32 s90, s50, 0x100
	v_add_u32_e32 v218, 0x80000, v241
	v_add_u32_e32 v220, 0x80000, v242
	v_mov_b32_e32 v219, v193
	v_mov_b32_e32 v221, v193
	s_addc_u32 s91, s51, 0
	s_mov_b32 s92, -2
	s_mov_b64 s[50:51], s[10:11]
.Lpeel_p1_h:
	v_add_u32_e32 v128, 0, v238
	v_add_u32_e32 v129, 0x10000, v128
	v_add_u32_e32 v140, 0x14000, v128
	ds_read_b128 v[144:147], v129
	ds_read_b128 v[148:151], v129 offset:1024
	ds_read_b128 v[152:155], v129 offset:2048
	ds_read_b128 v[156:159], v129 offset:3072
	ds_read_b128 v[128:131], v140
	ds_read_b128 v[132:135], v140 offset:1024
	ds_read_b128 v[136:139], v140 offset:2048
	ds_read_b128 v[140:143], v140 offset:3072
	s_cmp_eq_u32 s92, 28
	s_cselect_b64 s[12:13], -1, 0
	s_add_i32 m0, s31, 0xc000
	ds_read_b128 v[184:187], v240
	ds_read_b128 v[188:191], v240 offset:1024
	ds_read_b128 v[176:179], v240 offset:2048
	ds_read_b128 v[180:183], v240 offset:3072
	ds_read_b128 v[168:171], v240 offset:4096
	ds_read_b128 v[172:175], v240 offset:5120
	ds_read_b128 v[160:163], v240 offset:6144
	ds_read_b128 v[164:167], v240 offset:7168
	global_load_lds_dwordx4 v214, s[50:51]
	s_add_i32 m0, s31, 0xe000
	s_and_b64 s[94:95], s[38:39], s[12:13]
	global_load_lds_dwordx4 v216, s[50:51]
	s_andn2_b64 vcc, exec, s[94:95]
	s_cbranch_vccz .Lpeel_p1_a
	v_mov_b32_e32 v215, v193
	v_mov_b32_e32 v217, v193
	v_mov_b64_e32 v[222:223], v[216:217]
	v_mov_b64_e32 v[224:225], v[214:215]
	s_branch .Lpeel_p1_b
.Lpeel_p1_a:
	v_mov_b64_e32 v[222:223], v[220:221]
	v_mov_b64_e32 v[224:225], v[218:219]
	v_mov_b32_e32 v212, v242
	v_mov_b32_e32 v192, v241
	v_mov_b32_e32 v216, v220
	v_mov_b32_e32 v214, v218
.Lpeel_p1_b:
	s_waitcnt vmcnt(8)
	s_add_u32 s93, s50, 0x80
	s_waitcnt lgkmcnt(0)
	s_addc_u32 s94, s51, 0
	s_and_b64 s[12:13], s[12:13], exec
	s_cselect_b32 s13, s5, s94
	s_cselect_b32 s12, s4, s93
	s_cselect_b32 s95, s47, s91
	s_cselect_b32 s94, s85, s90
	s_barrier
	s_setprio 1
	s_waitcnt lgkmcnt(0)
	v_mfma_f32_16x16x32_bf16 v[124:127], v[144:147], v[184:187], 0
	v_mfma_f32_16x16x32_bf16 v[120:123], v[152:155], v[184:187], 0
	v_mfma_f32_16x16x32_bf16 v[116:119], v[144:147], v[176:179], 0
	v_mfma_f32_16x16x32_bf16 v[112:115], v[152:155], v[176:179], 0
	v_mfma_f32_16x16x32_bf16 v[100:103], v[144:147], v[168:171], 0
	v_mfma_f32_16x16x32_bf16 v[96:99], v[152:155], v[168:171], 0
	v_mfma_f32_16x16x32_bf16 v[84:87], v[144:147], v[160:163], 0
	v_mfma_f32_16x16x32_bf16 v[80:83], v[152:155], v[160:163], 0
	v_mfma_f32_16x16x32_bf16 v[124:127], v[148:151], v[188:191], v[124:127]
	v_mfma_f32_16x16x32_bf16 v[120:123], v[156:159], v[188:191], v[120:123]
	v_mfma_f32_16x16x32_bf16 v[116:119], v[148:151], v[180:183], v[116:119]
	v_mfma_f32_16x16x32_bf16 v[112:115], v[156:159], v[180:183], v[112:115]
	v_mfma_f32_16x16x32_bf16 v[100:103], v[148:151], v[172:175], v[100:103]
	v_mfma_f32_16x16x32_bf16 v[96:99], v[156:159], v[172:175], v[96:99]
	v_mfma_f32_16x16x32_bf16 v[84:87], v[148:151], v[164:167], v[84:87]
	v_mfma_f32_16x16x32_bf16 v[80:83], v[156:159], v[164:167], v[80:83]
	s_setprio 0
	s_setprio 1
	v_mfma_f32_16x16x32_bf16 v[108:111], v[128:131], v[184:187], 0
	v_mfma_f32_16x16x32_bf16 v[104:107], v[136:139], v[184:187], 0
	v_mfma_f32_16x16x32_bf16 v[92:95], v[128:131], v[176:179], 0
	v_mfma_f32_16x16x32_bf16 v[88:91], v[136:139], v[176:179], 0
	v_mfma_f32_16x16x32_bf16 v[76:79], v[128:131], v[168:171], 0
	v_mfma_f32_16x16x32_bf16 v[72:75], v[136:139], v[168:171], 0
	v_mfma_f32_16x16x32_bf16 v[68:71], v[128:131], v[160:163], 0
	v_mfma_f32_16x16x32_bf16 v[64:67], v[136:139], v[160:163], 0
	v_mfma_f32_16x16x32_bf16 v[108:111], v[132:135], v[188:191], v[108:111]
	v_mfma_f32_16x16x32_bf16 v[104:107], v[140:143], v[188:191], v[104:107]
	v_mfma_f32_16x16x32_bf16 v[92:95], v[132:135], v[180:183], v[92:95]
	v_mfma_f32_16x16x32_bf16 v[88:91], v[140:143], v[180:183], v[88:91]
	v_mfma_f32_16x16x32_bf16 v[76:79], v[132:135], v[172:175], v[76:79]
	v_mfma_f32_16x16x32_bf16 v[72:75], v[140:143], v[172:175], v[72:75]
	v_mfma_f32_16x16x32_bf16 v[68:71], v[132:135], v[164:167], v[68:71]
	v_mfma_f32_16x16x32_bf16 v[64:67], v[140:143], v[164:167], v[64:67]
	s_setprio 0
	s_barrier
	s_mov_b32 m0, s34
	v_lshl_add_u64 v[196:197], s[94:95], 0, v[208:209]
	ds_read_b128 v[160:163], v240 offset:16384
	ds_read_b128 v[164:167], v240 offset:17408
	ds_read_b128 v[168:171], v240 offset:18432
	ds_read_b128 v[172:175], v240 offset:19456
	ds_read_b128 v[176:179], v240 offset:20480
	ds_read_b128 v[180:183], v240 offset:21504
	ds_read_b128 v[184:187], v240 offset:22528
	ds_read_b128 v[188:191], v240 offset:23552
	global_load_lds_dwordx4 v[196:197], off
	v_lshl_add_u64 v[198:199], s[94:95], 0, v[204:205]
	s_mov_b32 m0, s35
	v_lshl_add_u64 v[200:201], s[94:95], 0, v[210:211]
	global_load_lds_dwordx4 v[198:199], off
	s_mov_b32 m0, s40
	v_lshl_add_u64 v[202:203], s[94:95], 0, v[206:207]
	global_load_lds_dwordx4 v[200:201], off
	s_mov_b32 m0, s41
	v_mov_b32_e32 v213, v193
	global_load_lds_dwordx4 v[202:203], off
	s_mov_b32 m0, s31
	v_lshl_add_u64 v[226:227], s[12:13], 0, v[192:193]
	global_load_lds_dwordx4 v192, s[12:13]
	s_mov_b32 m0, s53
	v_lshl_add_u64 v[228:229], s[12:13], 0, v[212:213]
	global_load_lds_dwordx4 v212, s[12:13]
	s_waitcnt vmcnt(8)
	s_waitcnt lgkmcnt(0)
	s_barrier
; #define PG8_STAGE(bufoff, gbase, voff) do { _Pragma("unroll") for (int _i = 0; _i < 2; ++_i) \
;         __builtin_amdgcn_global_load_lds((const unsigned*)((const char*)(gbase) + (voff)[_i]), (LAS unsigned*)(lds + (bufoff) + ldsw + _i * 8192), 16, 0, 0); } while (0)
; #define PG8_LDA(dst, b, h) do { _Pragma("unroll") for (int m = 0; m < 4; ++m) _Pragma("unroll") for (int k = 0; k < 2; ++k) dst[m][k] = *(const LAS bf16x8*)(lds + PG8_SA(b, h) + aoff + m * 2048 + k * KOFF); } while (0)
; #define PG8_LDB(dst, b, h) do { _Pragma("unroll") for (int n = 0; n < 2; ++n) _Pragma("unroll") for (int k = 0; k < 2; ++k) dst[n][k] = *(const LAS bf16x8*)(lds + PG8_SB(b, h) + boff + n * 2048 + k * KOFF); } while (0)
; #define PG8_WAIT_V(n) asm volatile("s_waitcnt vmcnt(" #n ")" ::: "memory")
; #define PG8_WAIT_L(n) asm volatile("s_waitcnt lgkmcnt(" #n ")" ::: "memory")
; #define PG8_BAR __builtin_amdgcn_s_barrier()
; #define PG8_SCHED __builtin_amdgcn_sched_barrier(0)
; template <class Epi, class Sched, bool GATHER, bool FP8 = false, bool ALIGN = true>
; __device__ __forceinline__ void gemm_phase(LAS unsigned char* lds, int wave, const Gemm g, const Sched& S, const Epi& E) {
;     ...
;             PG8_WAIT_V(8); PG8_WAIT_L(0); PG8_BAR; PG8_MMA(1, 0, At, B0); PG8_MMA(1, 1, At, B1); PG8_BAR; PG8_SCHED;
;             PG8_LDB(B0, 1, 0); PG8_LDB(B1, 1, 1); PG8_SCHED; PG8_LDA(At, 1, 0); PG8_STAGE(PG8_SA(0, 1), a2, ca1);
;             PG8_WAIT_V(8); PG8_WAIT_L(0); PG8_BAR; PG8_MMA(0, 0, At, B0); PG8_MMA(0, 1, At, B1); PG8_BAR; PG8_SCHED;
	s_setprio 1
	s_waitcnt lgkmcnt(0)
	v_mfma_f32_16x16x32_bf16 v[60:63], v[144:147], v[160:163], 0
	v_mfma_f32_16x16x32_bf16 v[56:59], v[152:155], v[160:163], 0
	v_mfma_f32_16x16x32_bf16 v[52:55], v[144:147], v[168:171], 0
	v_mfma_f32_16x16x32_bf16 v[48:51], v[152:155], v[168:171], 0
	v_mfma_f32_16x16x32_bf16 v[36:39], v[144:147], v[176:179], 0
	v_mfma_f32_16x16x32_bf16 v[32:35], v[152:155], v[176:179], 0
	v_mfma_f32_16x16x32_bf16 v[20:23], v[144:147], v[184:187], 0
	v_mfma_f32_16x16x32_bf16 v[16:19], v[152:155], v[184:187], 0
	v_mfma_f32_16x16x32_bf16 v[60:63], v[148:151], v[164:167], v[60:63]
	v_mfma_f32_16x16x32_bf16 v[56:59], v[156:159], v[164:167], v[56:59]
	v_mfma_f32_16x16x32_bf16 v[52:55], v[148:151], v[172:175], v[52:55]
	v_mfma_f32_16x16x32_bf16 v[48:51], v[156:159], v[172:175], v[48:51]
	v_mfma_f32_16x16x32_bf16 v[36:39], v[148:151], v[180:183], v[36:39]
	v_mfma_f32_16x16x32_bf16 v[32:35], v[156:159], v[180:183], v[32:35]
	v_mfma_f32_16x16x32_bf16 v[20:23], v[148:151], v[188:191], v[20:23]
	v_mfma_f32_16x16x32_bf16 v[16:19], v[156:159], v[188:191], v[16:19]
	s_setprio 0
	s_setprio 1
	v_mfma_f32_16x16x32_bf16 v[44:47], v[128:131], v[160:163], 0
	v_mfma_f32_16x16x32_bf16 v[40:43], v[136:139], v[160:163], 0
	v_mfma_f32_16x16x32_bf16 v[28:31], v[128:131], v[168:171], 0
	v_mfma_f32_16x16x32_bf16 v[24:27], v[136:139], v[168:171], 0
	v_mfma_f32_16x16x32_bf16 v[12:15], v[128:131], v[176:179], 0
	v_mfma_f32_16x16x32_bf16 v[8:11], v[136:139], v[176:179], 0
	v_mfma_f32_16x16x32_bf16 v[4:7], v[128:131], v[184:187], 0
	v_mfma_f32_16x16x32_bf16 v[0:3], v[136:139], v[184:187], 0
	v_mfma_f32_16x16x32_bf16 v[44:47], v[132:135], v[164:167], v[44:47]
	v_mfma_f32_16x16x32_bf16 v[40:43], v[140:143], v[164:167], v[40:43]
	v_mfma_f32_16x16x32_bf16 v[28:31], v[132:135], v[172:175], v[28:31]
	v_mfma_f32_16x16x32_bf16 v[24:27], v[140:143], v[172:175], v[24:27]
	v_mfma_f32_16x16x32_bf16 v[12:15], v[132:135], v[180:183], v[12:15]
	v_mfma_f32_16x16x32_bf16 v[8:11], v[140:143], v[180:183], v[8:11]
	v_mfma_f32_16x16x32_bf16 v[4:7], v[132:135], v[188:191], v[4:7]
	v_mfma_f32_16x16x32_bf16 v[0:3], v[140:143], v[188:191], v[0:3]
	s_setprio 0
	s_barrier
	s_add_i32 s93, 0, 0x18000
	s_add_i32 s94, 0, 0x1c000
	v_add_u32_e32 v140, s93, v238
	v_add_u32_e32 v156, s94, v238
	ds_read_b128 v[128:131], v140
	ds_read_b128 v[132:135], v140 offset:1024
	ds_read_b128 v[136:139], v140 offset:2048
	ds_read_b128 v[140:143], v140 offset:3072
	ds_read_b128 v[144:147], v156
	ds_read_b128 v[148:151], v156 offset:1024
	ds_read_b128 v[152:155], v156 offset:2048
	ds_read_b128 v[156:159], v156 offset:3072
	s_mov_b32 m0, s56
	v_lshl_add_u64 v[224:225], s[12:13], 0, v[224:225]
	ds_read_b128 v[160:163], v240 offset:32768
	ds_read_b128 v[164:167], v240 offset:33792
	ds_read_b128 v[168:171], v240 offset:34816
	ds_read_b128 v[172:175], v240 offset:35840
	ds_read_b128 v[176:179], v240 offset:36864
	ds_read_b128 v[180:183], v240 offset:37888
	ds_read_b128 v[184:187], v240 offset:38912
	ds_read_b128 v[188:191], v240 offset:39936
	global_load_lds_dwordx4 v[224:225], off
	v_lshl_add_u64 v[222:223], s[12:13], 0, v[222:223]
	s_mov_b32 m0, s57
	s_nop 0
	global_load_lds_dwordx4 v[222:223], off
	s_waitcnt vmcnt(8)
	s_waitcnt lgkmcnt(0)
	s_barrier
	s_setprio 1
	s_waitcnt lgkmcnt(0)
	v_mfma_f32_16x16x32_bf16 v[124:127], v[128:131], v[160:163], v[124:127]
	v_mfma_f32_16x16x32_bf16 v[120:123], v[136:139], v[160:163], v[120:123]
	v_mfma_f32_16x16x32_bf16 v[116:119], v[128:131], v[168:171], v[116:119]
	v_mfma_f32_16x16x32_bf16 v[112:115], v[136:139], v[168:171], v[112:115]
	v_mfma_f32_16x16x32_bf16 v[100:103], v[128:131], v[176:179], v[100:103]
	v_mfma_f32_16x16x32_bf16 v[96:99], v[136:139], v[176:179], v[96:99]
	v_mfma_f32_16x16x32_bf16 v[84:87], v[128:131], v[184:187], v[84:87]
	v_mfma_f32_16x16x32_bf16 v[80:83], v[136:139], v[184:187], v[80:83]
	v_mfma_f32_16x16x32_bf16 v[124:127], v[132:135], v[164:167], v[124:127]
	v_mfma_f32_16x16x32_bf16 v[120:123], v[140:143], v[164:167], v[120:123]
	v_mfma_f32_16x16x32_bf16 v[116:119], v[132:135], v[172:175], v[116:119]
	v_mfma_f32_16x16x32_bf16 v[112:115], v[140:143], v[172:175], v[112:115]
	v_mfma_f32_16x16x32_bf16 v[100:103], v[132:135], v[180:183], v[100:103]
	v_mfma_f32_16x16x32_bf16 v[96:99], v[140:143], v[180:183], v[96:99]
	v_mfma_f32_16x16x32_bf16 v[84:87], v[132:135], v[188:191], v[84:87]
	v_mfma_f32_16x16x32_bf16 v[80:83], v[140:143], v[188:191], v[80:83]
	s_setprio 0
	s_setprio 1
	v_mfma_f32_16x16x32_bf16 v[108:111], v[144:147], v[160:163], v[108:111]
	v_mfma_f32_16x16x32_bf16 v[104:107], v[152:155], v[160:163], v[104:107]
	v_mfma_f32_16x16x32_bf16 v[92:95], v[144:147], v[168:171], v[92:95]
	v_mfma_f32_16x16x32_bf16 v[88:91], v[152:155], v[168:171], v[88:91]
	v_mfma_f32_16x16x32_bf16 v[76:79], v[144:147], v[176:179], v[76:79]
	v_mfma_f32_16x16x32_bf16 v[72:75], v[152:155], v[176:179], v[72:75]
	v_mfma_f32_16x16x32_bf16 v[68:71], v[144:147], v[184:187], v[68:71]
	v_mfma_f32_16x16x32_bf16 v[64:67], v[152:155], v[184:187], v[64:67]
	v_mfma_f32_16x16x32_bf16 v[108:111], v[148:151], v[164:167], v[108:111]
	v_mfma_f32_16x16x32_bf16 v[104:107], v[156:159], v[164:167], v[104:107]
	v_mfma_f32_16x16x32_bf16 v[92:95], v[148:151], v[172:175], v[92:95]
	v_mfma_f32_16x16x32_bf16 v[88:91], v[156:159], v[172:175], v[88:91]
	v_mfma_f32_16x16x32_bf16 v[76:79], v[148:151], v[180:183], v[76:79]
	v_mfma_f32_16x16x32_bf16 v[72:75], v[156:159], v[180:183], v[72:75]
	v_mfma_f32_16x16x32_bf16 v[68:71], v[148:151], v[188:191], v[68:71]
	v_mfma_f32_16x16x32_bf16 v[64:67], v[156:159], v[188:191], v[64:67]
	s_setprio 0
	s_barrier
; #define PG8_STAGE(bufoff, gbase, voff) do { _Pragma("unroll") for (int _i = 0; _i < 2; ++_i) \
;         __builtin_amdgcn_global_load_lds((const unsigned*)((const char*)(gbase) + (voff)[_i]), (LAS unsigned*)(lds + (bufoff) + ldsw + _i * 8192), 16, 0, 0); } while (0)
; #define PG8_LDA(dst, b, h) do { _Pragma("unroll") for (int m = 0; m < 4; ++m) _Pragma("unroll") for (int k = 0; k < 2; ++k) dst[m][k] = *(const LAS bf16x8*)(lds + PG8_SA(b, h) + aoff + m * 2048 + k * KOFF); } while (0)
; #define PG8_WAIT_V(n) asm volatile("s_waitcnt vmcnt(" #n ")" ::: "memory")
; #define PG8_WAIT_L(n) asm volatile("s_waitcnt lgkmcnt(" #n ")" ::: "memory")
; #define PG8_BAR __builtin_amdgcn_s_barrier()
; #define PG8_SCHED __builtin_amdgcn_sched_barrier(0)
; template <class Epi, class Sched, bool GATHER, bool FP8 = false, bool ALIGN = true>
; __device__ __forceinline__ void gemm_phase(LAS unsigned char* lds, int wave, const Gemm g, const Sched& S, const Epi& E) {
;     ...
;         for (int t = 0; t < nt; t += 2) {
;             const bool last = (t == nt - 2);
;             const char* a1 = Ab + (size_t)(t + 1) * kstep;
;             const char* a2 = last ? Ab : Ab + (size_t)(t + 2) * kstep; const char* b2 = last ? nB : cB + (size_t)(t + 2) * kstep;
;             const char* a3 = a2 + kstep; const char* b3 = b2 + kstep;
;     ...
;             PG8_LDA(At, 1, 1); PG8_STAGE(PG8_SB(1, 0), b3, voffB0); PG8_STAGE(PG8_SB(1, 1), b3, voffB1); PG8_STAGE(PG8_SA(1, 0), a3, ca0);
;             PG8_WAIT_V(8); PG8_WAIT_L(0); PG8_BAR; PG8_MMA(1, 0, At, B0); PG8_MMA(1, 1, At, B1); PG8_BAR; PG8_SCHED;
	s_add_i32 s12, s93, s29
	v_lshl_add_u64 v[196:197], v[196:197], 0, s[62:63]
	s_mov_b32 m0, s12
	ds_read_b128 v[160:163], v240 offset:49152
	ds_read_b128 v[164:167], v240 offset:50176
	ds_read_b128 v[168:171], v240 offset:51200
	ds_read_b128 v[172:175], v240 offset:52224
	ds_read_b128 v[176:179], v240 offset:53248
	ds_read_b128 v[180:183], v240 offset:54272
	ds_read_b128 v[184:187], v240 offset:55296
	ds_read_b128 v[188:191], v240 offset:56320
	global_load_lds_dwordx4 v[196:197], off
	v_lshl_add_u64 v[196:197], v[198:199], 0, s[62:63]
	s_add_i32 m0, s12, 0x2000
	s_add_i32 s12, s94, s29
	global_load_lds_dwordx4 v[196:197], off
	v_lshl_add_u64 v[196:197], v[200:201], 0, s[62:63]
	s_mov_b32 m0, s12
	s_nop 0
	global_load_lds_dwordx4 v[196:197], off
	v_lshl_add_u64 v[196:197], v[202:203], 0, s[62:63]
	s_add_i32 m0, s12, 0x2000
	s_nop 0
	global_load_lds_dwordx4 v[196:197], off
	v_lshl_add_u64 v[196:197], v[226:227], 0, s[62:63]
	s_mov_b32 m0, s60
	s_nop 0
	global_load_lds_dwordx4 v[196:197], off
	v_lshl_add_u64 v[196:197], v[228:229], 0, s[62:63]
	s_mov_b32 m0, s73
	s_nop 0
	global_load_lds_dwordx4 v[196:197], off
	s_waitcnt vmcnt(8)
	s_waitcnt lgkmcnt(0)
	s_barrier
	s_setprio 1
	s_waitcnt lgkmcnt(0)
	v_mfma_f32_16x16x32_bf16 v[60:63], v[128:131], v[160:163], v[60:63]
	v_mfma_f32_16x16x32_bf16 v[56:59], v[136:139], v[160:163], v[56:59]
	v_mfma_f32_16x16x32_bf16 v[52:55], v[128:131], v[168:171], v[52:55]
	v_mfma_f32_16x16x32_bf16 v[48:51], v[136:139], v[168:171], v[48:51]
	v_mfma_f32_16x16x32_bf16 v[36:39], v[128:131], v[176:179], v[36:39]
	v_mfma_f32_16x16x32_bf16 v[32:35], v[136:139], v[176:179], v[32:35]
	v_mfma_f32_16x16x32_bf16 v[20:23], v[128:131], v[184:187], v[20:23]
	v_mfma_f32_16x16x32_bf16 v[16:19], v[136:139], v[184:187], v[16:19]
	v_mfma_f32_16x16x32_bf16 v[60:63], v[132:135], v[164:167], v[60:63]
	v_mfma_f32_16x16x32_bf16 v[56:59], v[140:143], v[164:167], v[56:59]
	v_mfma_f32_16x16x32_bf16 v[52:55], v[132:135], v[172:175], v[52:55]
	v_mfma_f32_16x16x32_bf16 v[48:51], v[140:143], v[172:175], v[48:51]
	v_mfma_f32_16x16x32_bf16 v[36:39], v[132:135], v[180:183], v[36:39]
	v_mfma_f32_16x16x32_bf16 v[32:35], v[140:143], v[180:183], v[32:35]
	v_mfma_f32_16x16x32_bf16 v[20:23], v[132:135], v[188:191], v[20:23]
	v_mfma_f32_16x16x32_bf16 v[16:19], v[140:143], v[188:191], v[16:19]
	s_setprio 0
	s_setprio 1
	v_mfma_f32_16x16x32_bf16 v[44:47], v[144:147], v[160:163], v[44:47]
	v_mfma_f32_16x16x32_bf16 v[40:43], v[152:155], v[160:163], v[40:43]
	v_mfma_f32_16x16x32_bf16 v[28:31], v[144:147], v[168:171], v[28:31]
	v_mfma_f32_16x16x32_bf16 v[24:27], v[152:155], v[168:171], v[24:27]
	v_mfma_f32_16x16x32_bf16 v[12:15], v[144:147], v[176:179], v[12:15]
	v_mfma_f32_16x16x32_bf16 v[8:11], v[152:155], v[176:179], v[8:11]
	v_mfma_f32_16x16x32_bf16 v[4:7], v[144:147], v[184:187], v[4:7]
	v_mfma_f32_16x16x32_bf16 v[0:3], v[152:155], v[184:187], v[0:3]
	v_mfma_f32_16x16x32_bf16 v[44:47], v[148:151], v[164:167], v[44:47]
	v_mfma_f32_16x16x32_bf16 v[40:43], v[156:159], v[164:167], v[40:43]
	v_mfma_f32_16x16x32_bf16 v[28:31], v[148:151], v[172:175], v[28:31]
	v_mfma_f32_16x16x32_bf16 v[24:27], v[156:159], v[172:175], v[24:27]
	v_mfma_f32_16x16x32_bf16 v[12:15], v[148:151], v[180:183], v[12:15]
	v_mfma_f32_16x16x32_bf16 v[8:11], v[156:159], v[180:183], v[8:11]
	v_mfma_f32_16x16x32_bf16 v[4:7], v[148:151], v[188:191], v[4:7]
	v_mfma_f32_16x16x32_bf16 v[0:3], v[156:159], v[188:191], v[0:3]
	s_setprio 0
	s_barrier
	s_add_i32 s92, s92, 2
	s_add_u32 s50, s50, 0x100
	s_addc_u32 s51, s51, 0
	s_add_u32 s90, s90, 0x100
	s_addc_u32 s91, s91, 0
	s_cmp_gt_u32 s92, 29
	s_cbranch_scc1 .LBB0_409
	s_branch .LBB0_407

; #define PG8_STAGE(bufoff, gbase, voff) do { _Pragma("unroll") for (int _i = 0; _i < 2; ++_i) \
;         __builtin_amdgcn_global_load_lds((const unsigned*)((const char*)(gbase) + (voff)[_i]), (LAS unsigned*)(lds + (bufoff) + ldsw + _i * 8192), 16, 0, 0); } while (0)
; #define PG8_LDA(dst, b, h) do { _Pragma("unroll") for (int m = 0; m < 4; ++m) _Pragma("unroll") for (int k = 0; k < 2; ++k) dst[m][k] = *(const LAS bf16x8*)(lds + PG8_SA(b, h) + aoff + m * 2048 + k * KOFF); } while (0)
; #define PG8_LDB(dst, b, h) do { _Pragma("unroll") for (int n = 0; n < 2; ++n) _Pragma("unroll") for (int k = 0; k < 2; ++k) dst[n][k] = *(const LAS bf16x8*)(lds + PG8_SB(b, h) + boff + n * 2048 + k * KOFF); } while (0)
; #define PG8_WAIT_V(n) asm volatile("s_waitcnt vmcnt(" #n ")" ::: "memory")
; #define PG8_WAIT_L(n) asm volatile("s_waitcnt lgkmcnt(" #n ")" ::: "memory")
; template <class Epi, class Sched, bool GATHER, bool FP8 = false, bool ALIGN = true>
; __device__ __forceinline__ void gemm_phase(LAS unsigned char* lds, int wave, const Gemm g, const Sched& S, const Epi& E) {
;     ...
;         const bool has_next = S.next(ui + 1, nxt);
;         const char* nB = has_next ? (const char*)g.Bt + (size_t)nxt.e * g.b_estride + (size_t)nxt.pn * tstep : cB;
; #pragma unroll 1
;         for (int t = 0; t < nt; t += 2) {
;             const bool last = (t == nt - 2);
;             const char* a1 = Ab + (size_t)(t + 1) * kstep;
;             const char* a2 = last ? Ab : Ab + (size_t)(t + 2) * kstep; const char* b2 = last ? nB : cB + (size_t)(t + 2) * kstep;
;             const char* a3 = a2 + kstep; const char* b3 = b2 + kstep;
;             PG8_LDB(B0, 0, 0); PG8_LDB(B1, 0, 1); PG8_SCHED; PG8_LDA(At, 0, 0); PG8_STAGE(PG8_SA(1, 1), a1, ca1);
;             if (last && has_next) PG8_AOFF(nxt, ca0, ca1);
;             PG8_WAIT_V(8); PG8_WAIT_L(0); PG8_BAR; PG8_MMA(0, 0, At, B0); PG8_MMA(0, 1, At, B1); PG8_BAR; PG8_SCHED;
;             PG8_LDA(At, 0, 1); PG8_STAGE(PG8_SB(0, 0), b2, voffB0); PG8_STAGE(PG8_SB(0, 1), b2, voffB1); PG8_STAGE(PG8_SA(0, 0), a2, ca0);
;     ...
;         for (int a = 0; a < 2; ++a)
; #pragma unroll
;             for (int b = 0; b < 2; ++b)
; #pragma unroll
;                 for (int m = 0; m < 4; ++m)
; #pragma unroll
;                     for (int n = 0; n < 2; ++n) acc[a][b][m][n] = (f32x4){0.f, 0.f, 0.f, 0.f};
;         cur = nxt; cB = nB; ++ui;
.LBB0_725:
	s_ashr_i32 s5, s4, 31
	s_lshl_b64 s[6:7], s[4:5], 20
	s_add_u32 s6, s13, s6
	s_addc_u32 s7, s14, s7
	s_and_b64 s[10:11], s[36:37], exec
	s_cselect_b32 s5, s7, s9
	s_cselect_b32 s79, s6, s8
	s_lshl_b32 s10, s59, 20
	v_add_u32_e32 v241, s10, v235
	v_add_u32_e32 v242, s10, v236
	s_add_u32 s80, s8, 0x100
	v_add_u32_e32 v218, 0x80000, v241
	v_add_u32_e32 v220, 0x80000, v242
	v_mov_b32_e32 v219, v193
	v_mov_b32_e32 v221, v193
	s_addc_u32 s81, s9, 0
	s_mov_b32 s82, -2
	s_mov_b64 s[8:9], s[48:49]
.Lpeel_out_h:
	v_add_u32_e32 v128, 0, v238
	v_add_u32_e32 v129, 0x10000, v128
	v_add_u32_e32 v140, 0x14000, v128
	ds_read_b128 v[144:147], v129
	ds_read_b128 v[148:151], v129 offset:1024
	ds_read_b128 v[152:155], v129 offset:2048
	ds_read_b128 v[156:159], v129 offset:3072
	ds_read_b128 v[128:131], v140
	ds_read_b128 v[132:135], v140 offset:1024
	ds_read_b128 v[136:139], v140 offset:2048
	ds_read_b128 v[140:143], v140 offset:3072
	s_cmp_eq_u32 s82, 28
	s_cselect_b64 s[10:11], -1, 0
	s_add_i32 m0, s24, 0xc000
	ds_read_b128 v[184:187], v240
	ds_read_b128 v[188:191], v240 offset:1024
	ds_read_b128 v[176:179], v240 offset:2048
	ds_read_b128 v[180:183], v240 offset:3072
	ds_read_b128 v[168:171], v240 offset:4096
	ds_read_b128 v[172:175], v240 offset:5120
	ds_read_b128 v[160:163], v240 offset:6144
	ds_read_b128 v[164:167], v240 offset:7168
	global_load_lds_dwordx4 v214, s[8:9]
	s_add_i32 m0, s24, 0xe000
	s_and_b64 s[84:85], s[36:37], s[10:11]
	global_load_lds_dwordx4 v216, s[8:9]
	s_andn2_b64 vcc, exec, s[84:85]
	s_cbranch_vccz .Lpeel_out_a
	v_mov_b32_e32 v215, v193
	v_mov_b32_e32 v217, v193
	v_mov_b64_e32 v[222:223], v[216:217]
	v_mov_b64_e32 v[224:225], v[214:215]
	s_branch .Lpeel_out_b
.Lpeel_out_a:
	v_mov_b64_e32 v[222:223], v[220:221]
	v_mov_b64_e32 v[224:225], v[218:219]
	v_mov_b32_e32 v212, v242
	v_mov_b32_e32 v192, v241
	v_mov_b32_e32 v216, v220
	v_mov_b32_e32 v214, v218
.Lpeel_out_b:
	s_waitcnt vmcnt(8)
	s_add_u32 s83, s8, 0x80
	s_waitcnt lgkmcnt(0)
	s_addc_u32 s84, s9, 0
	s_and_b64 s[10:11], s[10:11], exec
	s_cselect_b32 s11, s39, s84
	s_cselect_b32 s10, s38, s83
	s_cselect_b32 s85, s5, s81
	s_cselect_b32 s84, s79, s80
	s_barrier
	s_setprio 1
	s_waitcnt lgkmcnt(0)
	v_mfma_f32_16x16x32_bf16 v[124:127], v[144:147], v[184:187], 0
	v_mfma_f32_16x16x32_bf16 v[120:123], v[152:155], v[184:187], 0
	v_mfma_f32_16x16x32_bf16 v[108:111], v[144:147], v[176:179], 0
	v_mfma_f32_16x16x32_bf16 v[104:107], v[152:155], v[176:179], 0
	v_mfma_f32_16x16x32_bf16 v[92:95], v[144:147], v[168:171], 0
	v_mfma_f32_16x16x32_bf16 v[88:91], v[152:155], v[168:171], 0
	v_mfma_f32_16x16x32_bf16 v[76:79], v[144:147], v[160:163], 0
	v_mfma_f32_16x16x32_bf16 v[72:75], v[152:155], v[160:163], 0
	v_mfma_f32_16x16x32_bf16 v[124:127], v[148:151], v[188:191], v[124:127]
	v_mfma_f32_16x16x32_bf16 v[120:123], v[156:159], v[188:191], v[120:123]
	v_mfma_f32_16x16x32_bf16 v[108:111], v[148:151], v[180:183], v[108:111]
	v_mfma_f32_16x16x32_bf16 v[104:107], v[156:159], v[180:183], v[104:107]
	v_mfma_f32_16x16x32_bf16 v[92:95], v[148:151], v[172:175], v[92:95]
	v_mfma_f32_16x16x32_bf16 v[88:91], v[156:159], v[172:175], v[88:91]
	v_mfma_f32_16x16x32_bf16 v[76:79], v[148:151], v[164:167], v[76:79]
	v_mfma_f32_16x16x32_bf16 v[72:75], v[156:159], v[164:167], v[72:75]
	s_setprio 0
	s_setprio 1
	v_mfma_f32_16x16x32_bf16 v[116:119], v[128:131], v[184:187], 0
	v_mfma_f32_16x16x32_bf16 v[112:115], v[136:139], v[184:187], 0
	v_mfma_f32_16x16x32_bf16 v[100:103], v[128:131], v[176:179], 0
	v_mfma_f32_16x16x32_bf16 v[96:99], v[136:139], v[176:179], 0
	v_mfma_f32_16x16x32_bf16 v[84:87], v[128:131], v[168:171], 0
	v_mfma_f32_16x16x32_bf16 v[80:83], v[136:139], v[168:171], 0
	v_mfma_f32_16x16x32_bf16 v[68:71], v[128:131], v[160:163], 0
	v_mfma_f32_16x16x32_bf16 v[64:67], v[136:139], v[160:163], 0
	v_mfma_f32_16x16x32_bf16 v[116:119], v[132:135], v[188:191], v[116:119]
	v_mfma_f32_16x16x32_bf16 v[112:115], v[140:143], v[188:191], v[112:115]
	v_mfma_f32_16x16x32_bf16 v[100:103], v[132:135], v[180:183], v[100:103]
	v_mfma_f32_16x16x32_bf16 v[96:99], v[140:143], v[180:183], v[96:99]
	v_mfma_f32_16x16x32_bf16 v[84:87], v[132:135], v[172:175], v[84:87]
	v_mfma_f32_16x16x32_bf16 v[80:83], v[140:143], v[172:175], v[80:83]
	v_mfma_f32_16x16x32_bf16 v[68:71], v[132:135], v[164:167], v[68:71]
	v_mfma_f32_16x16x32_bf16 v[64:67], v[140:143], v[164:167], v[64:67]
	s_setprio 0
	s_barrier
	s_mov_b32 m0, s29
	v_lshl_add_u64 v[196:197], s[84:85], 0, v[208:209]
	ds_read_b128 v[160:163], v240 offset:16384
	ds_read_b128 v[164:167], v240 offset:17408
	ds_read_b128 v[168:171], v240 offset:18432
	ds_read_b128 v[172:175], v240 offset:19456
	ds_read_b128 v[176:179], v240 offset:20480
	ds_read_b128 v[180:183], v240 offset:21504
	ds_read_b128 v[184:187], v240 offset:22528
	ds_read_b128 v[188:191], v240 offset:23552
	global_load_lds_dwordx4 v[196:197], off
	v_lshl_add_u64 v[198:199], s[84:85], 0, v[204:205]
	s_mov_b32 m0, s30
	v_lshl_add_u64 v[200:201], s[84:85], 0, v[210:211]
	global_load_lds_dwordx4 v[198:199], off
	s_mov_b32 m0, s31
	v_lshl_add_u64 v[202:203], s[84:85], 0, v[206:207]
	global_load_lds_dwordx4 v[200:201], off
	s_mov_b32 m0, s34
	v_mov_b32_e32 v213, v193
	global_load_lds_dwordx4 v[202:203], off
	s_mov_b32 m0, s24
	v_lshl_add_u64 v[226:227], s[10:11], 0, v[192:193]
	global_load_lds_dwordx4 v192, s[10:11]
	s_mov_b32 m0, s35
	v_lshl_add_u64 v[228:229], s[10:11], 0, v[212:213]
	global_load_lds_dwordx4 v212, s[10:11]
	s_waitcnt vmcnt(8)
	s_waitcnt lgkmcnt(0)
	s_barrier
; #define PG8_STAGE(bufoff, gbase, voff) do { _Pragma("unroll") for (int _i = 0; _i < 2; ++_i) \
;         __builtin_amdgcn_global_load_lds((const unsigned*)((const char*)(gbase) + (voff)[_i]), (LAS unsigned*)(lds + (bufoff) + ldsw + _i * 8192), 16, 0, 0); } while (0)
; #define PG8_LDA(dst, b, h) do { _Pragma("unroll") for (int m = 0; m < 4; ++m) _Pragma("unroll") for (int k = 0; k < 2; ++k) dst[m][k] = *(const LAS bf16x8*)(lds + PG8_SA(b, h) + aoff + m * 2048 + k * KOFF); } while (0)
; #define PG8_LDB(dst, b, h) do { _Pragma("unroll") for (int n = 0; n < 2; ++n) _Pragma("unroll") for (int k = 0; k < 2; ++k) dst[n][k] = *(const LAS bf16x8*)(lds + PG8_SB(b, h) + boff + n * 2048 + k * KOFF); } while (0)
; #define PG8_WAIT_V(n) asm volatile("s_waitcnt vmcnt(" #n ")" ::: "memory")
; #define PG8_WAIT_L(n) asm volatile("s_waitcnt lgkmcnt(" #n ")" ::: "memory")
; #define PG8_BAR __builtin_amdgcn_s_barrier()
; #define PG8_SCHED __builtin_amdgcn_sched_barrier(0)
; template <class Epi, class Sched, bool GATHER, bool FP8 = false, bool ALIGN = true>
; __device__ __forceinline__ void gemm_phase(LAS unsigned char* lds, int wave, const Gemm g, const Sched& S, const Epi& E) {
;     ...
;             PG8_WAIT_V(8); PG8_WAIT_L(0); PG8_BAR; PG8_MMA(1, 0, At, B0); PG8_MMA(1, 1, At, B1); PG8_BAR; PG8_SCHED;
;             PG8_LDB(B0, 1, 0); PG8_LDB(B1, 1, 1); PG8_SCHED; PG8_LDA(At, 1, 0); PG8_STAGE(PG8_SA(0, 1), a2, ca1);
;             PG8_WAIT_V(8); PG8_WAIT_L(0); PG8_BAR; PG8_MMA(0, 0, At, B0); PG8_MMA(0, 1, At, B1); PG8_BAR; PG8_SCHED;
	s_setprio 1
	s_waitcnt lgkmcnt(0)
	v_mfma_f32_16x16x32_bf16 v[60:63], v[144:147], v[160:163], 0
	v_mfma_f32_16x16x32_bf16 v[56:59], v[152:155], v[160:163], 0
	v_mfma_f32_16x16x32_bf16 v[44:47], v[144:147], v[168:171], 0
	v_mfma_f32_16x16x32_bf16 v[40:43], v[152:155], v[168:171], 0
	v_mfma_f32_16x16x32_bf16 v[28:31], v[144:147], v[176:179], 0
	v_mfma_f32_16x16x32_bf16 v[24:27], v[152:155], v[176:179], 0
	v_mfma_f32_16x16x32_bf16 v[12:15], v[144:147], v[184:187], 0
	v_mfma_f32_16x16x32_bf16 v[8:11], v[152:155], v[184:187], 0
	v_mfma_f32_16x16x32_bf16 v[60:63], v[148:151], v[164:167], v[60:63]
	v_mfma_f32_16x16x32_bf16 v[56:59], v[156:159], v[164:167], v[56:59]
	v_mfma_f32_16x16x32_bf16 v[44:47], v[148:151], v[172:175], v[44:47]
	v_mfma_f32_16x16x32_bf16 v[40:43], v[156:159], v[172:175], v[40:43]
	v_mfma_f32_16x16x32_bf16 v[28:31], v[148:151], v[180:183], v[28:31]
	v_mfma_f32_16x16x32_bf16 v[24:27], v[156:159], v[180:183], v[24:27]
	v_mfma_f32_16x16x32_bf16 v[12:15], v[148:151], v[188:191], v[12:15]
	v_mfma_f32_16x16x32_bf16 v[8:11], v[156:159], v[188:191], v[8:11]
	s_setprio 0
	s_setprio 1
	v_mfma_f32_16x16x32_bf16 v[52:55], v[128:131], v[160:163], 0
	v_mfma_f32_16x16x32_bf16 v[48:51], v[136:139], v[160:163], 0
	v_mfma_f32_16x16x32_bf16 v[36:39], v[128:131], v[168:171], 0
	v_mfma_f32_16x16x32_bf16 v[32:35], v[136:139], v[168:171], 0
	v_mfma_f32_16x16x32_bf16 v[20:23], v[128:131], v[176:179], 0
	v_mfma_f32_16x16x32_bf16 v[16:19], v[136:139], v[176:179], 0
	v_mfma_f32_16x16x32_bf16 v[4:7], v[128:131], v[184:187], 0
	v_mfma_f32_16x16x32_bf16 v[0:3], v[136:139], v[184:187], 0
	v_mfma_f32_16x16x32_bf16 v[52:55], v[132:135], v[164:167], v[52:55]
	v_mfma_f32_16x16x32_bf16 v[48:51], v[140:143], v[164:167], v[48:51]
	v_mfma_f32_16x16x32_bf16 v[36:39], v[132:135], v[172:175], v[36:39]
	v_mfma_f32_16x16x32_bf16 v[32:35], v[140:143], v[172:175], v[32:35]
	v_mfma_f32_16x16x32_bf16 v[20:23], v[132:135], v[180:183], v[20:23]
	v_mfma_f32_16x16x32_bf16 v[16:19], v[140:143], v[180:183], v[16:19]
	v_mfma_f32_16x16x32_bf16 v[4:7], v[132:135], v[188:191], v[4:7]
	v_mfma_f32_16x16x32_bf16 v[0:3], v[140:143], v[188:191], v[0:3]
	s_setprio 0
	s_barrier
	s_add_i32 s83, 0, 0x18000
	s_add_i32 s84, 0, 0x1c000
	v_add_u32_e32 v140, s83, v238
	v_add_u32_e32 v156, s84, v238
	ds_read_b128 v[128:131], v140
	ds_read_b128 v[132:135], v140 offset:1024
	ds_read_b128 v[136:139], v140 offset:2048
	ds_read_b128 v[140:143], v140 offset:3072
	ds_read_b128 v[144:147], v156
	ds_read_b128 v[148:151], v156 offset:1024
	ds_read_b128 v[152:155], v156 offset:2048
	ds_read_b128 v[156:159], v156 offset:3072
	s_mov_b32 m0, s40
	v_lshl_add_u64 v[224:225], s[10:11], 0, v[224:225]
	ds_read_b128 v[160:163], v240 offset:32768
	ds_read_b128 v[164:167], v240 offset:33792
	ds_read_b128 v[168:171], v240 offset:34816
	ds_read_b128 v[172:175], v240 offset:35840
	ds_read_b128 v[176:179], v240 offset:36864
	ds_read_b128 v[180:183], v240 offset:37888
	ds_read_b128 v[184:187], v240 offset:38912
	ds_read_b128 v[188:191], v240 offset:39936
	global_load_lds_dwordx4 v[224:225], off
	v_lshl_add_u64 v[222:223], s[10:11], 0, v[222:223]
	s_mov_b32 m0, s41
	s_nop 0
	global_load_lds_dwordx4 v[222:223], off
	s_waitcnt vmcnt(8)
	s_waitcnt lgkmcnt(0)
	s_barrier
	s_setprio 1
	s_waitcnt lgkmcnt(0)
	v_mfma_f32_16x16x32_bf16 v[124:127], v[128:131], v[160:163], v[124:127]
	v_mfma_f32_16x16x32_bf16 v[120:123], v[136:139], v[160:163], v[120:123]
	v_mfma_f32_16x16x32_bf16 v[108:111], v[128:131], v[168:171], v[108:111]
	v_mfma_f32_16x16x32_bf16 v[104:107], v[136:139], v[168:171], v[104:107]
	v_mfma_f32_16x16x32_bf16 v[92:95], v[128:131], v[176:179], v[92:95]
	v_mfma_f32_16x16x32_bf16 v[88:91], v[136:139], v[176:179], v[88:91]
	v_mfma_f32_16x16x32_bf16 v[76:79], v[128:131], v[184:187], v[76:79]
	v_mfma_f32_16x16x32_bf16 v[72:75], v[136:139], v[184:187], v[72:75]
	v_mfma_f32_16x16x32_bf16 v[124:127], v[132:135], v[164:167], v[124:127]
	v_mfma_f32_16x16x32_bf16 v[120:123], v[140:143], v[164:167], v[120:123]
	v_mfma_f32_16x16x32_bf16 v[108:111], v[132:135], v[172:175], v[108:111]
	v_mfma_f32_16x16x32_bf16 v[104:107], v[140:143], v[172:175], v[104:107]
	v_mfma_f32_16x16x32_bf16 v[92:95], v[132:135], v[180:183], v[92:95]
	v_mfma_f32_16x16x32_bf16 v[88:91], v[140:143], v[180:183], v[88:91]
	v_mfma_f32_16x16x32_bf16 v[76:79], v[132:135], v[188:191], v[76:79]
	v_mfma_f32_16x16x32_bf16 v[72:75], v[140:143], v[188:191], v[72:75]
	s_setprio 0
	s_setprio 1
	v_mfma_f32_16x16x32_bf16 v[116:119], v[144:147], v[160:163], v[116:119]
	v_mfma_f32_16x16x32_bf16 v[112:115], v[152:155], v[160:163], v[112:115]
	v_mfma_f32_16x16x32_bf16 v[100:103], v[144:147], v[168:171], v[100:103]
	v_mfma_f32_16x16x32_bf16 v[96:99], v[152:155], v[168:171], v[96:99]
	v_mfma_f32_16x16x32_bf16 v[84:87], v[144:147], v[176:179], v[84:87]
	v_mfma_f32_16x16x32_bf16 v[80:83], v[152:155], v[176:179], v[80:83]
	v_mfma_f32_16x16x32_bf16 v[68:71], v[144:147], v[184:187], v[68:71]
	v_mfma_f32_16x16x32_bf16 v[64:67], v[152:155], v[184:187], v[64:67]
	v_mfma_f32_16x16x32_bf16 v[116:119], v[148:151], v[164:167], v[116:119]
	v_mfma_f32_16x16x32_bf16 v[112:115], v[156:159], v[164:167], v[112:115]
	v_mfma_f32_16x16x32_bf16 v[100:103], v[148:151], v[172:175], v[100:103]
	v_mfma_f32_16x16x32_bf16 v[96:99], v[156:159], v[172:175], v[96:99]
	v_mfma_f32_16x16x32_bf16 v[84:87], v[148:151], v[180:183], v[84:87]
	v_mfma_f32_16x16x32_bf16 v[80:83], v[156:159], v[180:183], v[80:83]
	v_mfma_f32_16x16x32_bf16 v[68:71], v[148:151], v[188:191], v[68:71]
	v_mfma_f32_16x16x32_bf16 v[64:67], v[156:159], v[188:191], v[64:67]
	s_setprio 0
	s_barrier
; #define PG8_STAGE(bufoff, gbase, voff) do { _Pragma("unroll") for (int _i = 0; _i < 2; ++_i) \
;         __builtin_amdgcn_global_load_lds((const unsigned*)((const char*)(gbase) + (voff)[_i]), (LAS unsigned*)(lds + (bufoff) + ldsw + _i * 8192), 16, 0, 0); } while (0)
; #define PG8_LDA(dst, b, h) do { _Pragma("unroll") for (int m = 0; m < 4; ++m) _Pragma("unroll") for (int k = 0; k < 2; ++k) dst[m][k] = *(const LAS bf16x8*)(lds + PG8_SA(b, h) + aoff + m * 2048 + k * KOFF); } while (0)
; #define PG8_WAIT_V(n) asm volatile("s_waitcnt vmcnt(" #n ")" ::: "memory")
; #define PG8_WAIT_L(n) asm volatile("s_waitcnt lgkmcnt(" #n ")" ::: "memory")
; #define PG8_BAR __builtin_amdgcn_s_barrier()
; #define PG8_SCHED __builtin_amdgcn_sched_barrier(0)
; template <class Epi, class Sched, bool GATHER, bool FP8 = false, bool ALIGN = true>
; __device__ __forceinline__ void gemm_phase(LAS unsigned char* lds, int wave, const Gemm g, const Sched& S, const Epi& E) {
;     ...
;         for (int t = 0; t < nt; t += 2) {
;             const bool last = (t == nt - 2);
;             const char* a1 = Ab + (size_t)(t + 1) * kstep;
;             const char* a2 = last ? Ab : Ab + (size_t)(t + 2) * kstep; const char* b2 = last ? nB : cB + (size_t)(t + 2) * kstep;
;             const char* a3 = a2 + kstep; const char* b3 = b2 + kstep;
;     ...
;             PG8_LDA(At, 1, 1); PG8_STAGE(PG8_SB(1, 0), b3, voffB0); PG8_STAGE(PG8_SB(1, 1), b3, voffB1); PG8_STAGE(PG8_SA(1, 0), a3, ca0);
;             PG8_WAIT_V(8); PG8_WAIT_L(0); PG8_BAR; PG8_MMA(1, 0, At, B0); PG8_MMA(1, 1, At, B1); PG8_BAR; PG8_SCHED;
	s_add_i32 s10, s83, s15
	v_lshl_add_u64 v[196:197], v[196:197], 0, s[62:63]
	s_mov_b32 m0, s10
	ds_read_b128 v[160:163], v240 offset:49152
	ds_read_b128 v[164:167], v240 offset:50176
	ds_read_b128 v[168:171], v240 offset:51200
	ds_read_b128 v[172:175], v240 offset:52224
	ds_read_b128 v[176:179], v240 offset:53248
	ds_read_b128 v[180:183], v240 offset:54272
	ds_read_b128 v[184:187], v240 offset:55296
	ds_read_b128 v[188:191], v240 offset:56320
	global_load_lds_dwordx4 v[196:197], off
	v_lshl_add_u64 v[196:197], v[198:199], 0, s[62:63]
	s_add_i32 m0, s10, 0x2000
	s_add_i32 s10, s84, s15
	global_load_lds_dwordx4 v[196:197], off
	v_lshl_add_u64 v[196:197], v[200:201], 0, s[62:63]
	s_mov_b32 m0, s10
	s_nop 0
	global_load_lds_dwordx4 v[196:197], off
	v_lshl_add_u64 v[196:197], v[202:203], 0, s[62:63]
	s_add_i32 m0, s10, 0x2000
	s_nop 0
	global_load_lds_dwordx4 v[196:197], off
	v_lshl_add_u64 v[196:197], v[226:227], 0, s[62:63]
	s_mov_b32 m0, s56
	s_nop 0
	global_load_lds_dwordx4 v[196:197], off
	v_lshl_add_u64 v[196:197], v[228:229], 0, s[62:63]
	s_mov_b32 m0, s57
	s_nop 0
	global_load_lds_dwordx4 v[196:197], off
	s_waitcnt vmcnt(8)
	s_waitcnt lgkmcnt(0)
	s_barrier
	s_setprio 1
	s_waitcnt lgkmcnt(0)
	v_mfma_f32_16x16x32_bf16 v[60:63], v[128:131], v[160:163], v[60:63]
	v_mfma_f32_16x16x32_bf16 v[56:59], v[136:139], v[160:163], v[56:59]
	v_mfma_f32_16x16x32_bf16 v[44:47], v[128:131], v[168:171], v[44:47]
	v_mfma_f32_16x16x32_bf16 v[40:43], v[136:139], v[168:171], v[40:43]
	v_mfma_f32_16x16x32_bf16 v[28:31], v[128:131], v[176:179], v[28:31]
	v_mfma_f32_16x16x32_bf16 v[24:27], v[136:139], v[176:179], v[24:27]
	v_mfma_f32_16x16x32_bf16 v[12:15], v[128:131], v[184:187], v[12:15]
	v_mfma_f32_16x16x32_bf16 v[8:11], v[136:139], v[184:187], v[8:11]
	v_mfma_f32_16x16x32_bf16 v[60:63], v[132:135], v[164:167], v[60:63]
	v_mfma_f32_16x16x32_bf16 v[56:59], v[140:143], v[164:167], v[56:59]
	v_mfma_f32_16x16x32_bf16 v[44:47], v[132:135], v[172:175], v[44:47]
	v_mfma_f32_16x16x32_bf16 v[40:43], v[140:143], v[172:175], v[40:43]
	v_mfma_f32_16x16x32_bf16 v[28:31], v[132:135], v[180:183], v[28:31]
	v_mfma_f32_16x16x32_bf16 v[24:27], v[140:143], v[180:183], v[24:27]
	v_mfma_f32_16x16x32_bf16 v[12:15], v[132:135], v[188:191], v[12:15]
	v_mfma_f32_16x16x32_bf16 v[8:11], v[140:143], v[188:191], v[8:11]
	s_setprio 0
	s_setprio 1
	v_mfma_f32_16x16x32_bf16 v[52:55], v[144:147], v[160:163], v[52:55]
	v_mfma_f32_16x16x32_bf16 v[48:51], v[152:155], v[160:163], v[48:51]
	v_mfma_f32_16x16x32_bf16 v[36:39], v[144:147], v[168:171], v[36:39]
	v_mfma_f32_16x16x32_bf16 v[32:35], v[152:155], v[168:171], v[32:35]
	v_mfma_f32_16x16x32_bf16 v[20:23], v[144:147], v[176:179], v[20:23]
	v_mfma_f32_16x16x32_bf16 v[16:19], v[152:155], v[176:179], v[16:19]
	v_mfma_f32_16x16x32_bf16 v[4:7], v[144:147], v[184:187], v[4:7]
	v_mfma_f32_16x16x32_bf16 v[0:3], v[152:155], v[184:187], v[0:3]
	v_mfma_f32_16x16x32_bf16 v[52:55], v[148:151], v[164:167], v[52:55]
	v_mfma_f32_16x16x32_bf16 v[48:51], v[156:159], v[164:167], v[48:51]
	v_mfma_f32_16x16x32_bf16 v[36:39], v[148:151], v[172:175], v[36:39]
	v_mfma_f32_16x16x32_bf16 v[32:35], v[156:159], v[172:175], v[32:35]
	v_mfma_f32_16x16x32_bf16 v[20:23], v[148:151], v[180:183], v[20:23]
	v_mfma_f32_16x16x32_bf16 v[16:19], v[156:159], v[180:183], v[16:19]
	v_mfma_f32_16x16x32_bf16 v[4:7], v[148:151], v[188:191], v[4:7]
	v_mfma_f32_16x16x32_bf16 v[0:3], v[156:159], v[188:191], v[0:3]
	s_setprio 0
	s_barrier
	s_add_i32 s82, s82, 2
	s_add_u32 s8, s8, 0x100
	s_addc_u32 s9, s9, 0
	s_add_u32 s80, s80, 0x100
	s_addc_u32 s81, s81, 0
	s_cmp_gt_u32 s82, 29
	s_cbranch_scc1 .LBB0_730
	s_branch .LBB0_728

; #define PG8_STAGE(bufoff, gbase, voff) do { _Pragma("unroll") for (int _i = 0; _i < 2; ++_i) \
;         __builtin_amdgcn_global_load_lds((const unsigned*)((const char*)(gbase) + (voff)[_i]), (LAS unsigned*)(lds + (bufoff) + ldsw + _i * 8192), 16, 0, 0); } while (0)
; #define PG8_LDA(dst, b, h) do { _Pragma("unroll") for (int m = 0; m < 4; ++m) _Pragma("unroll") for (int k = 0; k < 2; ++k) dst[m][k] = *(const LAS bf16x8*)(lds + PG8_SA(b, h) + aoff + m * 2048 + k * KOFF); } while (0)
; #define PG8_LDB(dst, b, h) do { _Pragma("unroll") for (int n = 0; n < 2; ++n) _Pragma("unroll") for (int k = 0; k < 2; ++k) dst[n][k] = *(const LAS bf16x8*)(lds + PG8_SB(b, h) + boff + n * 2048 + k * KOFF); } while (0)
; #define PG8_WAIT_V(n) asm volatile("s_waitcnt vmcnt(" #n ")" ::: "memory")
; #define PG8_WAIT_L(n) asm volatile("s_waitcnt lgkmcnt(" #n ")" ::: "memory")
; template <class Epi, class Sched, bool GATHER, bool FP8 = false, bool ALIGN = true>
; __device__ __forceinline__ void gemm_phase(LAS unsigned char* lds, int wave, const Gemm g, const Sched& S, const Epi& E) {
;     ...
;         const bool has_next = S.next(ui + 1, nxt);
;         const char* nB = has_next ? (const char*)g.Bt + (size_t)nxt.e * g.b_estride + (size_t)nxt.pn * tstep : cB;
; #pragma unroll 1
;         for (int t = 0; t < nt; t += 2) {
;             const bool last = (t == nt - 2);
;             const char* a1 = Ab + (size_t)(t + 1) * kstep;
;             const char* a2 = last ? Ab : Ab + (size_t)(t + 2) * kstep; const char* b2 = last ? nB : cB + (size_t)(t + 2) * kstep;
;             const char* a3 = a2 + kstep; const char* b3 = b2 + kstep;
;             PG8_LDB(B0, 0, 0); PG8_LDB(B1, 0, 1); PG8_SCHED; PG8_LDA(At, 0, 0); PG8_STAGE(PG8_SA(1, 1), a1, ca1);
;             if (last && has_next) PG8_AOFF(nxt, ca0, ca1);
;             PG8_WAIT_V(8); PG8_WAIT_L(0); PG8_BAR; PG8_MMA(0, 0, At, B0); PG8_MMA(0, 1, At, B1); PG8_BAR; PG8_SCHED;
;             PG8_LDA(At, 0, 1); PG8_STAGE(PG8_SB(0, 0), b2, voffB0); PG8_STAGE(PG8_SB(0, 1), b2, voffB1); PG8_STAGE(PG8_SA(0, 0), a2, ca0);
;     ...
;         for (int a = 0; a < 2; ++a)
; #pragma unroll
;             for (int b = 0; b < 2; ++b)
; #pragma unroll
;                 for (int m = 0; m < 4; ++m)
; #pragma unroll
;                     for (int n = 0; n < 2; ++n) acc[a][b][m][n] = (f32x4){0.f, 0.f, 0.f, 0.f};
;         cur = nxt; cB = nB; ++ui;
.LBB0_1078:
	s_ashr_i32 s5, s4, 31
	s_lshl_b64 s[12:13], s[4:5], 21
	s_add_u32 s5, s24, s12
	s_addc_u32 s9, s29, s13
	s_ashr_i32 s49, s48, 31
	s_lshl_b64 s[12:13], s[48:49], 19
	s_add_u32 s80, s5, s12
	s_addc_u32 s81, s9, s13
	s_and_b64 s[12:13], s[50:51], exec
	s_cselect_b32 s5, s81, s11
	s_cselect_b32 s9, s80, s10
	s_lshl_b32 s12, s73, 8
	v_add_u32_e32 v0, s12, v222
	v_ashrrev_i32_e32 v1, 31, v0
	v_lshl_add_u64 v[218:219], v[0:1], 2, s[36:37]
	v_add_u32_e32 v0, s12, v223
	v_ashrrev_i32_e32 v1, 31, v0
	s_add_u32 s49, s10, 0x100
	v_lshl_add_u64 v[220:221], v[0:1], 2, s[36:37]
	s_addc_u32 s82, s11, 0
	s_mov_b32 s83, -2
	s_mov_b64 s[10:11], s[44:45]
.Lpeel_gu_h:
	v_add_u32_e32 v0, 0, v236
	v_add_u32_e32 v1, 0x10000, v0
	v_add_u32_e32 v12, 0x14000, v0
	ds_read_b128 v[16:19], v1
	ds_read_b128 v[20:23], v1 offset:1024
	ds_read_b128 v[24:27], v1 offset:2048
	ds_read_b128 v[28:31], v1 offset:3072
	ds_read_b128 v[0:3], v12
	ds_read_b128 v[4:7], v12 offset:1024
	ds_read_b128 v[8:11], v12 offset:2048
	ds_read_b128 v[12:15], v12 offset:3072
	s_cmp_eq_u32 s83, 12
	s_cselect_b64 s[12:13], -1, 0
	s_add_i32 m0, s31, 0xc000
	ds_read_b128 v[56:59], v238
	ds_read_b128 v[60:63], v238 offset:1024
	ds_read_b128 v[48:51], v238 offset:2048
	ds_read_b128 v[52:55], v238 offset:3072
	ds_read_b128 v[40:43], v238 offset:4096
	ds_read_b128 v[44:47], v238 offset:5120
	ds_read_b128 v[32:35], v238 offset:6144
	ds_read_b128 v[36:39], v238 offset:7168
	global_load_lds_dwordx4 v212, s[10:11]
	s_add_i32 m0, s31, 0xe000
	s_and_b64 s[14:15], s[50:51], s[12:13]
	global_load_lds_dwordx4 v216, s[10:11]
	s_andn2_b64 vcc, exec, s[14:15]
	s_cbranch_vccz .Lpeel_gu_a
	v_mov_b32_e32 v213, v193
	s_branch .Lpeel_gu_b
.Lpeel_gu_a:
	global_load_dword v192, v[218:219], off
	global_load_dword v196, v[218:219], off offset:512
	global_load_dword v197, v[220:221], off
	global_load_dword v198, v[220:221], off offset:512
	v_mov_b32_e32 v213, v193
	s_waitcnt vmcnt(0)
	v_lshl_add_u32 v192, v192, 11, v224
	v_lshl_add_u32 v212, v196, 11, v224
	v_lshl_add_u32 v214, v197, 11, v225
	v_lshl_add_u32 v216, v198, 11, v225
.Lpeel_gu_b:
	s_waitcnt vmcnt(8)
	s_add_u32 s14, s10, 0x80
	s_waitcnt lgkmcnt(0)
	s_addc_u32 s15, s11, 0
	s_and_b64 s[12:13], s[12:13], exec
	v_mov_b32_e32 v217, v193
	s_cselect_b32 s13, s7, s15
	s_cselect_b32 s12, s6, s14
	s_cselect_b32 s15, s5, s82
	s_cselect_b32 s14, s9, s49
	s_barrier
	s_setprio 1
	s_waitcnt lgkmcnt(0)
	v_mfma_scale_f32_16x16x128_f8f6f4 v[188:191], v[16:23], v[56:63], 0, v252, v251 op_sel_hi:[0,0,0]
	v_mfma_scale_f32_16x16x128_f8f6f4 v[180:183], v[24:31], v[56:63], 0, v252, v251 op_sel_hi:[0,0,0]
	v_mfma_scale_f32_16x16x128_f8f6f4 v[172:175], v[16:23], v[48:55], 0, v252, v251 op_sel_hi:[0,0,0]
	v_mfma_scale_f32_16x16x128_f8f6f4 v[164:167], v[24:31], v[48:55], 0, v252, v251 op_sel_hi:[0,0,0]
	v_mfma_scale_f32_16x16x128_f8f6f4 v[156:159], v[16:23], v[40:47], 0, v252, v251 op_sel_hi:[0,0,0]
	v_mfma_scale_f32_16x16x128_f8f6f4 v[148:151], v[24:31], v[40:47], 0, v252, v251 op_sel_hi:[0,0,0]
	v_mfma_scale_f32_16x16x128_f8f6f4 v[140:143], v[16:23], v[32:39], 0, v252, v251 op_sel_hi:[0,0,0]
	v_mfma_scale_f32_16x16x128_f8f6f4 v[132:135], v[24:31], v[32:39], 0, v252, v251 op_sel_hi:[0,0,0]
	s_setprio 0
	s_setprio 1
	v_mfma_scale_f32_16x16x128_f8f6f4 v[184:187], v[0:7], v[56:63], 0, v252, v251 op_sel_hi:[0,0,0]
	v_mfma_scale_f32_16x16x128_f8f6f4 v[176:179], v[8:15], v[56:63], 0, v252, v251 op_sel_hi:[0,0,0]
	v_mfma_scale_f32_16x16x128_f8f6f4 v[168:171], v[0:7], v[48:55], 0, v252, v251 op_sel_hi:[0,0,0]
	v_mfma_scale_f32_16x16x128_f8f6f4 v[160:163], v[8:15], v[48:55], 0, v252, v251 op_sel_hi:[0,0,0]
	v_mfma_scale_f32_16x16x128_f8f6f4 v[152:155], v[0:7], v[40:47], 0, v252, v251 op_sel_hi:[0,0,0]
	v_mfma_scale_f32_16x16x128_f8f6f4 v[144:147], v[8:15], v[40:47], 0, v252, v251 op_sel_hi:[0,0,0]
	v_mfma_scale_f32_16x16x128_f8f6f4 v[136:139], v[0:7], v[32:39], 0, v252, v251 op_sel_hi:[0,0,0]
	v_mfma_scale_f32_16x16x128_f8f6f4 v[128:131], v[8:15], v[32:39], 0, v252, v251 op_sel_hi:[0,0,0]
	s_setprio 0
	s_barrier
	s_mov_b32 m0, s34
	v_lshl_add_u64 v[196:197], s[14:15], 0, v[204:205]
	ds_read_b128 v[32:35], v238 offset:16384
	ds_read_b128 v[36:39], v238 offset:17408
	ds_read_b128 v[40:43], v238 offset:18432
	ds_read_b128 v[44:47], v238 offset:19456
	ds_read_b128 v[48:51], v238 offset:20480
	ds_read_b128 v[52:55], v238 offset:21504
	ds_read_b128 v[56:59], v238 offset:22528
	ds_read_b128 v[60:63], v238 offset:23552
	global_load_lds_dwordx4 v[196:197], off
	v_lshl_add_u64 v[198:199], s[14:15], 0, v[208:209]
	s_mov_b32 m0, s35
	v_lshl_add_u64 v[200:201], s[14:15], 0, v[206:207]
	global_load_lds_dwordx4 v[198:199], off
	s_mov_b32 m0, s40
	v_lshl_add_u64 v[202:203], s[14:15], 0, v[210:211]
	global_load_lds_dwordx4 v[200:201], off
	s_mov_b32 m0, s41
	v_mov_b32_e32 v215, v193
	global_load_lds_dwordx4 v[202:203], off
	s_mov_b32 m0, s31
	v_lshl_add_u64 v[226:227], s[12:13], 0, v[192:193]
	global_load_lds_dwordx4 v192, s[12:13]
	s_mov_b32 m0, s53
	v_lshl_add_u64 v[228:229], s[12:13], 0, v[214:215]
	global_load_lds_dwordx4 v214, s[12:13]
	s_waitcnt vmcnt(8)
	s_waitcnt lgkmcnt(0)
	s_barrier
; #define PG8_STAGE(bufoff, gbase, voff) do { _Pragma("unroll") for (int _i = 0; _i < 2; ++_i) \
;         __builtin_amdgcn_global_load_lds((const unsigned*)((const char*)(gbase) + (voff)[_i]), (LAS unsigned*)(lds + (bufoff) + ldsw + _i * 8192), 16, 0, 0); } while (0)
; #define PG8_LDA(dst, b, h) do { _Pragma("unroll") for (int m = 0; m < 4; ++m) _Pragma("unroll") for (int k = 0; k < 2; ++k) dst[m][k] = *(const LAS bf16x8*)(lds + PG8_SA(b, h) + aoff + m * 2048 + k * KOFF); } while (0)
; #define PG8_LDB(dst, b, h) do { _Pragma("unroll") for (int n = 0; n < 2; ++n) _Pragma("unroll") for (int k = 0; k < 2; ++k) dst[n][k] = *(const LAS bf16x8*)(lds + PG8_SB(b, h) + boff + n * 2048 + k * KOFF); } while (0)
; #define PG8_WAIT_V(n) asm volatile("s_waitcnt vmcnt(" #n ")" ::: "memory")
; #define PG8_WAIT_L(n) asm volatile("s_waitcnt lgkmcnt(" #n ")" ::: "memory")
; #define PG8_BAR __builtin_amdgcn_s_barrier()
; #define PG8_SCHED __builtin_amdgcn_sched_barrier(0)
; template <class Epi, class Sched, bool GATHER, bool FP8 = false, bool ALIGN = true>
; __device__ __forceinline__ void gemm_phase(LAS unsigned char* lds, int wave, const Gemm g, const Sched& S, const Epi& E) {
;     ...
;             PG8_WAIT_V(8); PG8_WAIT_L(0); PG8_BAR; PG8_MMA(1, 0, At, B0); PG8_MMA(1, 1, At, B1); PG8_BAR; PG8_SCHED;
;             PG8_LDB(B0, 1, 0); PG8_LDB(B1, 1, 1); PG8_SCHED; PG8_LDA(At, 1, 0); PG8_STAGE(PG8_SA(0, 1), a2, ca1);
;             PG8_WAIT_V(8); PG8_WAIT_L(0); PG8_BAR; PG8_MMA(0, 0, At, B0); PG8_MMA(0, 1, At, B1); PG8_BAR; PG8_SCHED;
;             PG8_LDA(At, 1, 1); PG8_STAGE(PG8_SB(1, 0), b3, voffB0); PG8_STAGE(PG8_SB(1, 1), b3, voffB1); PG8_STAGE(PG8_SA(1, 0), a3, ca0);
	s_setprio 1
	s_waitcnt lgkmcnt(0)
	v_mfma_scale_f32_16x16x128_f8f6f4 v[124:127], v[16:23], v[32:39], 0, v252, v251 op_sel_hi:[0,0,0]
	v_mfma_scale_f32_16x16x128_f8f6f4 v[116:119], v[24:31], v[32:39], 0, v252, v251 op_sel_hi:[0,0,0]
	v_mfma_scale_f32_16x16x128_f8f6f4 v[108:111], v[16:23], v[40:47], 0, v252, v251 op_sel_hi:[0,0,0]
	v_mfma_scale_f32_16x16x128_f8f6f4 v[100:103], v[24:31], v[40:47], 0, v252, v251 op_sel_hi:[0,0,0]
	v_mfma_scale_f32_16x16x128_f8f6f4 v[92:95], v[16:23], v[48:55], 0, v252, v251 op_sel_hi:[0,0,0]
	v_mfma_scale_f32_16x16x128_f8f6f4 v[84:87], v[24:31], v[48:55], 0, v252, v251 op_sel_hi:[0,0,0]
	v_mfma_scale_f32_16x16x128_f8f6f4 v[76:79], v[16:23], v[56:63], 0, v252, v251 op_sel_hi:[0,0,0]
	v_mfma_scale_f32_16x16x128_f8f6f4 v[68:71], v[24:31], v[56:63], 0, v252, v251 op_sel_hi:[0,0,0]
	s_setprio 0
	s_setprio 1
	v_mfma_scale_f32_16x16x128_f8f6f4 v[120:123], v[0:7], v[32:39], 0, v252, v251 op_sel_hi:[0,0,0]
	v_mfma_scale_f32_16x16x128_f8f6f4 v[112:115], v[8:15], v[32:39], 0, v252, v251 op_sel_hi:[0,0,0]
	v_mfma_scale_f32_16x16x128_f8f6f4 v[104:107], v[0:7], v[40:47], 0, v252, v251 op_sel_hi:[0,0,0]
	v_mfma_scale_f32_16x16x128_f8f6f4 v[96:99], v[8:15], v[40:47], 0, v252, v251 op_sel_hi:[0,0,0]
	v_mfma_scale_f32_16x16x128_f8f6f4 v[88:91], v[0:7], v[48:55], 0, v252, v251 op_sel_hi:[0,0,0]
	v_mfma_scale_f32_16x16x128_f8f6f4 v[80:83], v[8:15], v[48:55], 0, v252, v251 op_sel_hi:[0,0,0]
	v_mfma_scale_f32_16x16x128_f8f6f4 v[72:75], v[0:7], v[56:63], 0, v252, v251 op_sel_hi:[0,0,0]
	v_mfma_scale_f32_16x16x128_f8f6f4 v[64:67], v[8:15], v[56:63], 0, v252, v251 op_sel_hi:[0,0,0]
	s_setprio 0
	s_barrier
	s_add_i32 s14, 0, 0x18000
	s_add_i32 s15, 0, 0x1c000
	v_add_u32_e32 v12, s14, v236
	v_add_u32_e32 v28, s15, v236
	ds_read_b128 v[0:3], v12
	ds_read_b128 v[4:7], v12 offset:1024
	ds_read_b128 v[8:11], v12 offset:2048
	ds_read_b128 v[12:15], v12 offset:3072
	ds_read_b128 v[16:19], v28
	ds_read_b128 v[20:23], v28 offset:1024
	ds_read_b128 v[24:27], v28 offset:2048
	ds_read_b128 v[28:31], v28 offset:3072
	s_mov_b32 m0, s56
	v_lshl_add_u64 v[230:231], s[12:13], 0, v[212:213]
	ds_read_b128 v[32:35], v238 offset:32768
	ds_read_b128 v[36:39], v238 offset:33792
	ds_read_b128 v[40:43], v238 offset:34816
	ds_read_b128 v[44:47], v238 offset:35840
	ds_read_b128 v[48:51], v238 offset:36864
	ds_read_b128 v[52:55], v238 offset:37888
	ds_read_b128 v[56:59], v238 offset:38912
	ds_read_b128 v[60:63], v238 offset:39936
	global_load_lds_dwordx4 v[230:231], off
	v_lshl_add_u64 v[230:231], s[12:13], 0, v[216:217]
	s_mov_b32 m0, s57
	s_nop 0
	global_load_lds_dwordx4 v[230:231], off
	s_waitcnt vmcnt(8)
	s_waitcnt lgkmcnt(0)
	s_barrier
	s_setprio 1
	s_waitcnt lgkmcnt(0)
	v_mfma_scale_f32_16x16x128_f8f6f4 v[188:191], v[0:7], v[32:39], v[188:191], v252, v251 op_sel_hi:[0,0,0]
	v_mfma_scale_f32_16x16x128_f8f6f4 v[180:183], v[8:15], v[32:39], v[180:183], v252, v251 op_sel_hi:[0,0,0]
	v_mfma_scale_f32_16x16x128_f8f6f4 v[172:175], v[0:7], v[40:47], v[172:175], v252, v251 op_sel_hi:[0,0,0]
	v_mfma_scale_f32_16x16x128_f8f6f4 v[164:167], v[8:15], v[40:47], v[164:167], v252, v251 op_sel_hi:[0,0,0]
	v_mfma_scale_f32_16x16x128_f8f6f4 v[156:159], v[0:7], v[48:55], v[156:159], v252, v251 op_sel_hi:[0,0,0]
	v_mfma_scale_f32_16x16x128_f8f6f4 v[148:151], v[8:15], v[48:55], v[148:151], v252, v251 op_sel_hi:[0,0,0]
	v_mfma_scale_f32_16x16x128_f8f6f4 v[140:143], v[0:7], v[56:63], v[140:143], v252, v251 op_sel_hi:[0,0,0]
	v_mfma_scale_f32_16x16x128_f8f6f4 v[132:135], v[8:15], v[56:63], v[132:135], v252, v251 op_sel_hi:[0,0,0]
	s_setprio 0
	s_setprio 1
	v_mfma_scale_f32_16x16x128_f8f6f4 v[184:187], v[16:23], v[32:39], v[184:187], v252, v251 op_sel_hi:[0,0,0]
	v_mfma_scale_f32_16x16x128_f8f6f4 v[176:179], v[24:31], v[32:39], v[176:179], v252, v251 op_sel_hi:[0,0,0]
	v_mfma_scale_f32_16x16x128_f8f6f4 v[168:171], v[16:23], v[40:47], v[168:171], v252, v251 op_sel_hi:[0,0,0]
	v_mfma_scale_f32_16x16x128_f8f6f4 v[160:163], v[24:31], v[40:47], v[160:163], v252, v251 op_sel_hi:[0,0,0]
	v_mfma_scale_f32_16x16x128_f8f6f4 v[152:155], v[16:23], v[48:55], v[152:155], v252, v251 op_sel_hi:[0,0,0]
	v_mfma_scale_f32_16x16x128_f8f6f4 v[144:147], v[24:31], v[48:55], v[144:147], v252, v251 op_sel_hi:[0,0,0]
	v_mfma_scale_f32_16x16x128_f8f6f4 v[136:139], v[16:23], v[56:63], v[136:139], v252, v251 op_sel_hi:[0,0,0]
	v_mfma_scale_f32_16x16x128_f8f6f4 v[128:131], v[24:31], v[56:63], v[128:131], v252, v251 op_sel_hi:[0,0,0]
	s_setprio 0
	s_barrier
; #define PG8_STAGE(bufoff, gbase, voff) do { _Pragma("unroll") for (int _i = 0; _i < 2; ++_i) \
;         __builtin_amdgcn_global_load_lds((const unsigned*)((const char*)(gbase) + (voff)[_i]), (LAS unsigned*)(lds + (bufoff) + ldsw + _i * 8192), 16, 0, 0); } while (0)
; #define PG8_LDA(dst, b, h) do { _Pragma("unroll") for (int m = 0; m < 4; ++m) _Pragma("unroll") for (int k = 0; k < 2; ++k) dst[m][k] = *(const LAS bf16x8*)(lds + PG8_SA(b, h) + aoff + m * 2048 + k * KOFF); } while (0)
; #define PG8_WAIT_V(n) asm volatile("s_waitcnt vmcnt(" #n ")" ::: "memory")
; #define PG8_WAIT_L(n) asm volatile("s_waitcnt lgkmcnt(" #n ")" ::: "memory")
; #define PG8_BAR __builtin_amdgcn_s_barrier()
; #define PG8_SCHED __builtin_amdgcn_sched_barrier(0)
; template <class Epi, class Sched, bool GATHER, bool FP8 = false, bool ALIGN = true>
; __device__ __forceinline__ void gemm_phase(LAS unsigned char* lds, int wave, const Gemm g, const Sched& S, const Epi& E) {
;     ...
;         for (int t = 0; t < nt; t += 2) {
;             const bool last = (t == nt - 2);
;             const char* a1 = Ab + (size_t)(t + 1) * kstep;
;             const char* a2 = last ? Ab : Ab + (size_t)(t + 2) * kstep; const char* b2 = last ? nB : cB + (size_t)(t + 2) * kstep;
;             const char* a3 = a2 + kstep; const char* b3 = b2 + kstep;
;     ...
;             PG8_LDA(At, 1, 1); PG8_STAGE(PG8_SB(1, 0), b3, voffB0); PG8_STAGE(PG8_SB(1, 1), b3, voffB1); PG8_STAGE(PG8_SA(1, 0), a3, ca0);
;             PG8_WAIT_V(8); PG8_WAIT_L(0); PG8_BAR; PG8_MMA(1, 0, At, B0); PG8_MMA(1, 1, At, B1); PG8_BAR; PG8_SCHED;
	s_add_i32 s12, s14, s30
	v_lshl_add_u64 v[196:197], v[196:197], 0, s[62:63]
	s_mov_b32 m0, s12
	ds_read_b128 v[32:35], v238 offset:49152
	ds_read_b128 v[36:39], v238 offset:50176
	ds_read_b128 v[40:43], v238 offset:51200
	ds_read_b128 v[44:47], v238 offset:52224
	ds_read_b128 v[48:51], v238 offset:53248
	ds_read_b128 v[52:55], v238 offset:54272
	ds_read_b128 v[56:59], v238 offset:55296
	ds_read_b128 v[60:63], v238 offset:56320
	global_load_lds_dwordx4 v[196:197], off
	v_lshl_add_u64 v[196:197], v[198:199], 0, s[62:63]
	s_add_i32 m0, s12, 0x2000
	s_add_i32 s12, s15, s30
	global_load_lds_dwordx4 v[196:197], off
	v_lshl_add_u64 v[196:197], v[200:201], 0, s[62:63]
	s_mov_b32 m0, s12
	s_nop 0
	global_load_lds_dwordx4 v[196:197], off
	v_lshl_add_u64 v[196:197], v[202:203], 0, s[62:63]
	s_add_i32 m0, s12, 0x2000
	s_nop 0
	global_load_lds_dwordx4 v[196:197], off
	v_lshl_add_u64 v[196:197], v[226:227], 0, s[62:63]
	s_mov_b32 m0, s58
	s_nop 0
	global_load_lds_dwordx4 v[196:197], off
	v_lshl_add_u64 v[196:197], v[228:229], 0, s[62:63]
	s_mov_b32 m0, s59
	s_nop 0
	global_load_lds_dwordx4 v[196:197], off
	s_waitcnt vmcnt(8)
	s_waitcnt lgkmcnt(0)
	s_barrier
	s_setprio 1
	s_waitcnt lgkmcnt(0)
	v_mfma_scale_f32_16x16x128_f8f6f4 v[124:127], v[0:7], v[32:39], v[124:127], v252, v251 op_sel_hi:[0,0,0]
	v_mfma_scale_f32_16x16x128_f8f6f4 v[116:119], v[8:15], v[32:39], v[116:119], v252, v251 op_sel_hi:[0,0,0]
	v_mfma_scale_f32_16x16x128_f8f6f4 v[108:111], v[0:7], v[40:47], v[108:111], v252, v251 op_sel_hi:[0,0,0]
	v_mfma_scale_f32_16x16x128_f8f6f4 v[100:103], v[8:15], v[40:47], v[100:103], v252, v251 op_sel_hi:[0,0,0]
	v_mfma_scale_f32_16x16x128_f8f6f4 v[92:95], v[0:7], v[48:55], v[92:95], v252, v251 op_sel_hi:[0,0,0]
	v_mfma_scale_f32_16x16x128_f8f6f4 v[84:87], v[8:15], v[48:55], v[84:87], v252, v251 op_sel_hi:[0,0,0]
	v_mfma_scale_f32_16x16x128_f8f6f4 v[76:79], v[0:7], v[56:63], v[76:79], v252, v251 op_sel_hi:[0,0,0]
	v_mfma_scale_f32_16x16x128_f8f6f4 v[68:71], v[8:15], v[56:63], v[68:71], v252, v251 op_sel_hi:[0,0,0]
	s_setprio 0
	s_setprio 1
	v_mfma_scale_f32_16x16x128_f8f6f4 v[120:123], v[16:23], v[32:39], v[120:123], v252, v251 op_sel_hi:[0,0,0]
	v_mfma_scale_f32_16x16x128_f8f6f4 v[112:115], v[24:31], v[32:39], v[112:115], v252, v251 op_sel_hi:[0,0,0]
	v_mfma_scale_f32_16x16x128_f8f6f4 v[104:107], v[16:23], v[40:47], v[104:107], v252, v251 op_sel_hi:[0,0,0]
	v_mfma_scale_f32_16x16x128_f8f6f4 v[96:99], v[24:31], v[40:47], v[96:99], v252, v251 op_sel_hi:[0,0,0]
	v_mfma_scale_f32_16x16x128_f8f6f4 v[88:91], v[16:23], v[48:55], v[88:91], v252, v251 op_sel_hi:[0,0,0]
	v_mfma_scale_f32_16x16x128_f8f6f4 v[80:83], v[24:31], v[48:55], v[80:83], v252, v251 op_sel_hi:[0,0,0]
	v_mfma_scale_f32_16x16x128_f8f6f4 v[72:75], v[16:23], v[56:63], v[72:75], v252, v251 op_sel_hi:[0,0,0]
	v_mfma_scale_f32_16x16x128_f8f6f4 v[64:67], v[24:31], v[56:63], v[64:67], v252, v251 op_sel_hi:[0,0,0]
	s_setprio 0
	s_barrier
	s_add_i32 s83, s83, 2
	s_add_u32 s10, s10, 0x100
	s_addc_u32 s11, s11, 0
	s_add_u32 s49, s49, 0x100
	s_addc_u32 s82, s82, 0
	s_cmp_gt_u32 s83, 13
	s_cbranch_scc1 .LBB0_1083
	s_branch .LBB0_1081

; template <class Epi, class Sched, bool GATHER, bool FP8 = false, bool ALIGN = true>
; __device__ __forceinline__ void gemm_phase(LAS unsigned char* lds, int wave, const Gemm g, const Sched& S, const Epi& E) {
;     ...
;         const bool has_next = S.next(ui + 1, nxt);
;         const char* nB = has_next ? (const char*)g.Bt + (size_t)nxt.e * g.b_estride + (size_t)nxt.pn * tstep : cB;
;     ...
;         for (int a = 0; a < 2; ++a)
; #pragma unroll
;             for (int b = 0; b < 2; ++b)
; #pragma unroll
;                 for (int m = 0; m < 4; ++m)
; #pragma unroll
;                     for (int n = 0; n < 2; ++n) acc[a][b][m][n] = (f32x4){0.f, 0.f, 0.f, 0.f};
;         cur = nxt; cB = nB; ++ui;
.LBB0_1154:
	s_ashr_i32 s5, s4, 31
	s_lshl_b64 s[12:13], s[4:5], 20
	s_add_u32 s5, s24, s12
	s_addc_u32 s14, s29, s13
	s_ashr_i32 s39, s38, 31
	s_lshl_b64 s[12:13], s[38:39], 17
	s_add_u32 s44, s5, s12
	s_addc_u32 s45, s14, s13
	s_and_b64 s[12:13], s[42:43], exec
	s_cselect_b32 s5, s45, s49
	s_cselect_b32 s39, s44, s48
	s_lshl_b32 s12, s60, 17
	v_add_u32_e32 v241, s12, v238
	v_add_u32_e32 v242, s12, v239
	v_add_u32_e32 v218, 0x10000, v241
	v_add_u32_e32 v220, 0x10000, v242
	v_mov_b32_e32 v219, v193
	v_mov_b32_e32 v221, v193
	s_mov_b64 s[82:83], 0
	s_mov_b64 s[84:85], -1
	s_mov_b64 s[80:81], 0

; #define PG8_STAGE(bufoff, gbase, voff) do { _Pragma("unroll") for (int _i = 0; _i < 2; ++_i) \
;         __builtin_amdgcn_global_load_lds((const unsigned*)((const char*)(gbase) + (voff)[_i]), (LAS unsigned*)(lds + (bufoff) + ldsw + _i * 8192), 16, 0, 0); } while (0)
; #define PG8_LDA(dst, b, h) do { _Pragma("unroll") for (int m = 0; m < 4; ++m) _Pragma("unroll") for (int k = 0; k < 2; ++k) dst[m][k] = *(const LAS bf16x8*)(lds + PG8_SA(b, h) + aoff + m * 2048 + k * KOFF); } while (0)
; #define PG8_LDB(dst, b, h) do { _Pragma("unroll") for (int n = 0; n < 2; ++n) _Pragma("unroll") for (int k = 0; k < 2; ++k) dst[n][k] = *(const LAS bf16x8*)(lds + PG8_SB(b, h) + boff + n * 2048 + k * KOFF); } while (0)
; #define PG8_WAIT_V(n) asm volatile("s_waitcnt vmcnt(" #n ")" ::: "memory")
; #define PG8_WAIT_L(n) asm volatile("s_waitcnt lgkmcnt(" #n ")" ::: "memory")
; #define PG8_BAR __builtin_amdgcn_s_barrier()
; #define PG8_SCHED __builtin_amdgcn_sched_barrier(0)
; template <class Epi, class Sched, bool GATHER, bool FP8 = false, bool ALIGN = true>
; __device__ __forceinline__ void gemm_phase(LAS unsigned char* lds, int wave, const Gemm g, const Sched& S, const Epi& E) {
;     ...
;             const char* a2 = last ? Ab : Ab + (size_t)(t + 2) * kstep; const char* b2 = last ? nB : cB + (size_t)(t + 2) * kstep;
;             const char* a3 = a2 + kstep; const char* b3 = b2 + kstep;
;             PG8_LDB(B0, 0, 0); PG8_LDB(B1, 0, 1); PG8_SCHED; PG8_LDA(At, 0, 0); PG8_STAGE(PG8_SA(1, 1), a1, ca1);
;             if (last && has_next) PG8_AOFF(nxt, ca0, ca1);
;             PG8_WAIT_V(8); PG8_WAIT_L(0); PG8_BAR; PG8_MMA(0, 0, At, B0); PG8_MMA(0, 1, At, B1); PG8_BAR; PG8_SCHED;
;             PG8_LDA(At, 0, 1); PG8_STAGE(PG8_SB(0, 0), b2, voffB0); PG8_STAGE(PG8_SB(0, 1), b2, voffB1); PG8_STAGE(PG8_SA(0, 0), a2, ca0);
;             PG8_WAIT_V(8); PG8_WAIT_L(0); PG8_BAR; PG8_MMA(1, 0, At, B0); PG8_MMA(1, 1, At, B1); PG8_BAR; PG8_SCHED;
;             PG8_LDB(B0, 1, 0); PG8_LDB(B1, 1, 1); PG8_SCHED; PG8_LDA(At, 1, 0); PG8_STAGE(PG8_SA(0, 1), a2, ca1);
.Lpeel_dn_b:
	s_xor_b64 s[50:51], s[84:85], -1
	s_add_u32 s14, s12, 0x100
	s_addc_u32 s15, s13, 0
	s_and_b64 s[12:13], s[80:81], exec
	s_cselect_b32 s13, s7, s15
	s_cselect_b32 s12, s6, s14
	s_add_u32 s14, s48, s82
	s_addc_u32 s15, s49, s83
	s_waitcnt vmcnt(8)
	s_add_u32 s79, s14, 0x100
	s_waitcnt lgkmcnt(0)
	s_addc_u32 s82, s15, 0
	s_and_b64 s[14:15], s[80:81], exec
	s_cselect_b32 s15, s5, s82
	s_cselect_b32 s14, s39, s79
	s_barrier
	s_setprio 1
	s_waitcnt lgkmcnt(0)
	v_mfma_scale_f32_16x16x128_f8f6f4 v[188:191], v[16:23], v[56:63], 0, v252, v251 op_sel_hi:[0,0,0]
	v_mfma_scale_f32_16x16x128_f8f6f4 v[184:187], v[24:31], v[56:63], 0, v252, v251 op_sel_hi:[0,0,0]
	v_mfma_scale_f32_16x16x128_f8f6f4 v[172:175], v[16:23], v[48:55], 0, v252, v251 op_sel_hi:[0,0,0]
	v_mfma_scale_f32_16x16x128_f8f6f4 v[168:171], v[24:31], v[48:55], 0, v252, v251 op_sel_hi:[0,0,0]
	v_mfma_scale_f32_16x16x128_f8f6f4 v[156:159], v[16:23], v[40:47], 0, v252, v251 op_sel_hi:[0,0,0]
	v_mfma_scale_f32_16x16x128_f8f6f4 v[152:155], v[24:31], v[40:47], 0, v252, v251 op_sel_hi:[0,0,0]
	v_mfma_scale_f32_16x16x128_f8f6f4 v[140:143], v[16:23], v[32:39], 0, v252, v251 op_sel_hi:[0,0,0]
	v_mfma_scale_f32_16x16x128_f8f6f4 v[136:139], v[24:31], v[32:39], 0, v252, v251 op_sel_hi:[0,0,0]
	s_setprio 0
	s_setprio 1
	v_mfma_scale_f32_16x16x128_f8f6f4 v[180:183], v[0:7], v[56:63], 0, v252, v251 op_sel_hi:[0,0,0]
	v_mfma_scale_f32_16x16x128_f8f6f4 v[176:179], v[8:15], v[56:63], 0, v252, v251 op_sel_hi:[0,0,0]
	v_mfma_scale_f32_16x16x128_f8f6f4 v[164:167], v[0:7], v[48:55], 0, v252, v251 op_sel_hi:[0,0,0]
	v_mfma_scale_f32_16x16x128_f8f6f4 v[160:163], v[8:15], v[48:55], 0, v252, v251 op_sel_hi:[0,0,0]
	v_mfma_scale_f32_16x16x128_f8f6f4 v[148:151], v[0:7], v[40:47], 0, v252, v251 op_sel_hi:[0,0,0]
	v_mfma_scale_f32_16x16x128_f8f6f4 v[144:147], v[8:15], v[40:47], 0, v252, v251 op_sel_hi:[0,0,0]
	v_mfma_scale_f32_16x16x128_f8f6f4 v[132:135], v[0:7], v[32:39], 0, v252, v251 op_sel_hi:[0,0,0]
	v_mfma_scale_f32_16x16x128_f8f6f4 v[128:131], v[8:15], v[32:39], 0, v252, v251 op_sel_hi:[0,0,0]
	s_setprio 0
	s_barrier
	s_mov_b32 m0, s34
	v_lshl_add_u64 v[196:197], s[14:15], 0, v[204:205]
	ds_read_b128 v[32:35], v240 offset:16384
	ds_read_b128 v[36:39], v240 offset:17408
	ds_read_b128 v[40:43], v240 offset:18432
	ds_read_b128 v[44:47], v240 offset:19456
	ds_read_b128 v[48:51], v240 offset:20480
	ds_read_b128 v[52:55], v240 offset:21504
	ds_read_b128 v[56:59], v240 offset:22528
	ds_read_b128 v[60:63], v240 offset:23552
	global_load_lds_dwordx4 v[196:197], off
	v_lshl_add_u64 v[198:199], s[14:15], 0, v[208:209]
	s_mov_b32 m0, s35
	v_lshl_add_u64 v[200:201], s[14:15], 0, v[206:207]
	global_load_lds_dwordx4 v[198:199], off
	s_mov_b32 m0, s40
	v_lshl_add_u64 v[202:203], s[14:15], 0, v[210:211]
	global_load_lds_dwordx4 v[200:201], off
	s_mov_b32 m0, s41
	v_mov_b32_e32 v213, v193
	global_load_lds_dwordx4 v[202:203], off
	s_mov_b32 m0, s31
	v_mov_b32_e32 v215, v193
	global_load_lds_dwordx4 v212, s[12:13]
	s_mov_b32 m0, s47
	v_lshl_add_u64 v[226:227], s[12:13], 0, v[212:213]
	global_load_lds_dwordx4 v214, s[12:13]
	s_waitcnt vmcnt(8)
	s_waitcnt lgkmcnt(0)
	v_lshl_add_u64 v[228:229], s[12:13], 0, v[214:215]
	s_barrier
	s_setprio 1
	s_waitcnt lgkmcnt(0)
	v_mfma_scale_f32_16x16x128_f8f6f4 v[124:127], v[16:23], v[32:39], 0, v252, v251 op_sel_hi:[0,0,0]
	v_mfma_scale_f32_16x16x128_f8f6f4 v[120:123], v[24:31], v[32:39], 0, v252, v251 op_sel_hi:[0,0,0]
	v_mfma_scale_f32_16x16x128_f8f6f4 v[108:111], v[16:23], v[40:47], 0, v252, v251 op_sel_hi:[0,0,0]
	v_mfma_scale_f32_16x16x128_f8f6f4 v[104:107], v[24:31], v[40:47], 0, v252, v251 op_sel_hi:[0,0,0]
	v_mfma_scale_f32_16x16x128_f8f6f4 v[92:95], v[16:23], v[48:55], 0, v252, v251 op_sel_hi:[0,0,0]
	v_mfma_scale_f32_16x16x128_f8f6f4 v[88:91], v[24:31], v[48:55], 0, v252, v251 op_sel_hi:[0,0,0]
	v_mfma_scale_f32_16x16x128_f8f6f4 v[76:79], v[16:23], v[56:63], 0, v252, v251 op_sel_hi:[0,0,0]
	v_mfma_scale_f32_16x16x128_f8f6f4 v[72:75], v[24:31], v[56:63], 0, v252, v251 op_sel_hi:[0,0,0]
	s_setprio 0
	s_setprio 1
	v_mfma_scale_f32_16x16x128_f8f6f4 v[116:119], v[0:7], v[32:39], 0, v252, v251 op_sel_hi:[0,0,0]
	v_mfma_scale_f32_16x16x128_f8f6f4 v[112:115], v[8:15], v[32:39], 0, v252, v251 op_sel_hi:[0,0,0]
	v_mfma_scale_f32_16x16x128_f8f6f4 v[100:103], v[0:7], v[40:47], 0, v252, v251 op_sel_hi:[0,0,0]
	v_mfma_scale_f32_16x16x128_f8f6f4 v[96:99], v[8:15], v[40:47], 0, v252, v251 op_sel_hi:[0,0,0]
	v_mfma_scale_f32_16x16x128_f8f6f4 v[84:87], v[0:7], v[48:55], 0, v252, v251 op_sel_hi:[0,0,0]
	v_mfma_scale_f32_16x16x128_f8f6f4 v[80:83], v[8:15], v[48:55], 0, v252, v251 op_sel_hi:[0,0,0]
	v_mfma_scale_f32_16x16x128_f8f6f4 v[68:71], v[0:7], v[56:63], 0, v252, v251 op_sel_hi:[0,0,0]
	v_mfma_scale_f32_16x16x128_f8f6f4 v[64:67], v[8:15], v[56:63], 0, v252, v251 op_sel_hi:[0,0,0]
	s_setprio 0
	s_barrier
	s_add_i32 s14, 0, 0x18000
	s_add_i32 s15, 0, 0x1c000
	v_add_u32_e32 v12, s14, v236
	v_add_u32_e32 v28, s15, v236
	ds_read_b128 v[0:3], v12
	ds_read_b128 v[4:7], v12 offset:1024
	ds_read_b128 v[8:11], v12 offset:2048
	ds_read_b128 v[12:15], v12 offset:3072
	ds_read_b128 v[16:19], v28
	ds_read_b128 v[20:23], v28 offset:1024
	ds_read_b128 v[24:27], v28 offset:2048
	ds_read_b128 v[28:31], v28 offset:3072
	s_mov_b32 m0, s53
	v_lshl_add_u64 v[224:225], s[12:13], 0, v[224:225]
	ds_read_b128 v[32:35], v240 offset:32768
	ds_read_b128 v[36:39], v240 offset:33792
	ds_read_b128 v[40:43], v240 offset:34816
	ds_read_b128 v[44:47], v240 offset:35840
	ds_read_b128 v[48:51], v240 offset:36864
	ds_read_b128 v[52:55], v240 offset:37888
	ds_read_b128 v[56:59], v240 offset:38912
	ds_read_b128 v[60:63], v240 offset:39936
	global_load_lds_dwordx4 v[224:225], off
	v_lshl_add_u64 v[222:223], s[12:13], 0, v[222:223]
	s_mov_b32 m0, s56
	s_nop 0
	global_load_lds_dwordx4 v[222:223], off
	s_waitcnt vmcnt(8)
	s_waitcnt lgkmcnt(0)
	s_barrier
; #define PG8_STAGE(bufoff, gbase, voff) do { _Pragma("unroll") for (int _i = 0; _i < 2; ++_i) \
;         __builtin_amdgcn_global_load_lds((const unsigned*)((const char*)(gbase) + (voff)[_i]), (LAS unsigned*)(lds + (bufoff) + ldsw + _i * 8192), 16, 0, 0); } while (0)
; #define PG8_LDA(dst, b, h) do { _Pragma("unroll") for (int m = 0; m < 4; ++m) _Pragma("unroll") for (int k = 0; k < 2; ++k) dst[m][k] = *(const LAS bf16x8*)(lds + PG8_SA(b, h) + aoff + m * 2048 + k * KOFF); } while (0)
; #define PG8_WAIT_V(n) asm volatile("s_waitcnt vmcnt(" #n ")" ::: "memory")
; #define PG8_WAIT_L(n) asm volatile("s_waitcnt lgkmcnt(" #n ")" ::: "memory")
; #define PG8_BAR __builtin_amdgcn_s_barrier()
; #define PG8_SCHED __builtin_amdgcn_sched_barrier(0)
; template <class Epi, class Sched, bool GATHER, bool FP8 = false, bool ALIGN = true>
; __device__ __forceinline__ void gemm_phase(LAS unsigned char* lds, int wave, const Gemm g, const Sched& S, const Epi& E) {
;     ...
;             PG8_WAIT_V(8); PG8_WAIT_L(0); PG8_BAR; PG8_MMA(0, 0, At, B0); PG8_MMA(0, 1, At, B1); PG8_BAR; PG8_SCHED;
;             PG8_LDA(At, 1, 1); PG8_STAGE(PG8_SB(1, 0), b3, voffB0); PG8_STAGE(PG8_SB(1, 1), b3, voffB1); PG8_STAGE(PG8_SA(1, 0), a3, ca0);
;             PG8_WAIT_V(8); PG8_WAIT_L(0); PG8_BAR; PG8_MMA(1, 0, At, B0); PG8_MMA(1, 1, At, B1); PG8_BAR; PG8_SCHED;
	s_setprio 1
	s_waitcnt lgkmcnt(0)
	v_mfma_scale_f32_16x16x128_f8f6f4 v[188:191], v[0:7], v[32:39], v[188:191], v252, v251 op_sel_hi:[0,0,0]
	v_mfma_scale_f32_16x16x128_f8f6f4 v[184:187], v[8:15], v[32:39], v[184:187], v252, v251 op_sel_hi:[0,0,0]
	v_mfma_scale_f32_16x16x128_f8f6f4 v[172:175], v[0:7], v[40:47], v[172:175], v252, v251 op_sel_hi:[0,0,0]
	v_mfma_scale_f32_16x16x128_f8f6f4 v[168:171], v[8:15], v[40:47], v[168:171], v252, v251 op_sel_hi:[0,0,0]
	v_mfma_scale_f32_16x16x128_f8f6f4 v[156:159], v[0:7], v[48:55], v[156:159], v252, v251 op_sel_hi:[0,0,0]
	v_mfma_scale_f32_16x16x128_f8f6f4 v[152:155], v[8:15], v[48:55], v[152:155], v252, v251 op_sel_hi:[0,0,0]
	v_mfma_scale_f32_16x16x128_f8f6f4 v[140:143], v[0:7], v[56:63], v[140:143], v252, v251 op_sel_hi:[0,0,0]
	v_mfma_scale_f32_16x16x128_f8f6f4 v[136:139], v[8:15], v[56:63], v[136:139], v252, v251 op_sel_hi:[0,0,0]
	s_setprio 0
	s_setprio 1
	v_mfma_scale_f32_16x16x128_f8f6f4 v[180:183], v[16:23], v[32:39], v[180:183], v252, v251 op_sel_hi:[0,0,0]
	v_mfma_scale_f32_16x16x128_f8f6f4 v[176:179], v[24:31], v[32:39], v[176:179], v252, v251 op_sel_hi:[0,0,0]
	v_mfma_scale_f32_16x16x128_f8f6f4 v[164:167], v[16:23], v[40:47], v[164:167], v252, v251 op_sel_hi:[0,0,0]
	v_mfma_scale_f32_16x16x128_f8f6f4 v[160:163], v[24:31], v[40:47], v[160:163], v252, v251 op_sel_hi:[0,0,0]
	v_mfma_scale_f32_16x16x128_f8f6f4 v[148:151], v[16:23], v[48:55], v[148:151], v252, v251 op_sel_hi:[0,0,0]
	v_mfma_scale_f32_16x16x128_f8f6f4 v[144:147], v[24:31], v[48:55], v[144:147], v252, v251 op_sel_hi:[0,0,0]
	v_mfma_scale_f32_16x16x128_f8f6f4 v[132:135], v[16:23], v[56:63], v[132:135], v252, v251 op_sel_hi:[0,0,0]
	v_mfma_scale_f32_16x16x128_f8f6f4 v[128:131], v[24:31], v[56:63], v[128:131], v252, v251 op_sel_hi:[0,0,0]
	s_setprio 0
	s_barrier
	s_add_i32 s12, s14, s30
	v_lshl_add_u64 v[196:197], v[196:197], 0, s[62:63]
	s_mov_b32 m0, s12
	ds_read_b128 v[32:35], v240 offset:49152
	ds_read_b128 v[36:39], v240 offset:50176
	ds_read_b128 v[40:43], v240 offset:51200
	ds_read_b128 v[44:47], v240 offset:52224
	ds_read_b128 v[48:51], v240 offset:53248
	ds_read_b128 v[52:55], v240 offset:54272
	ds_read_b128 v[56:59], v240 offset:55296
	ds_read_b128 v[60:63], v240 offset:56320
	global_load_lds_dwordx4 v[196:197], off
	v_lshl_add_u64 v[196:197], v[198:199], 0, s[62:63]
	s_add_i32 m0, s12, 0x2000
	s_add_i32 s12, s15, s30
	global_load_lds_dwordx4 v[196:197], off
	v_lshl_add_u64 v[196:197], v[200:201], 0, s[62:63]
	s_mov_b32 m0, s12
	s_nop 0
	global_load_lds_dwordx4 v[196:197], off
	v_lshl_add_u64 v[196:197], v[202:203], 0, s[62:63]
	s_add_i32 m0, s12, 0x2000
	s_nop 0
	global_load_lds_dwordx4 v[196:197], off
	v_lshl_add_u64 v[196:197], v[226:227], 0, s[62:63]
	s_mov_b32 m0, s57
	s_nop 0
	global_load_lds_dwordx4 v[196:197], off
	v_lshl_add_u64 v[196:197], v[228:229], 0, s[62:63]
	s_mov_b32 m0, s58
	s_nop 0
	global_load_lds_dwordx4 v[196:197], off
	s_waitcnt vmcnt(8)
	s_waitcnt lgkmcnt(0)
	s_barrier
	s_setprio 1
	s_waitcnt lgkmcnt(0)
	v_mfma_scale_f32_16x16x128_f8f6f4 v[124:127], v[0:7], v[32:39], v[124:127], v252, v251 op_sel_hi:[0,0,0]
	v_mfma_scale_f32_16x16x128_f8f6f4 v[120:123], v[8:15], v[32:39], v[120:123], v252, v251 op_sel_hi:[0,0,0]
	v_mfma_scale_f32_16x16x128_f8f6f4 v[108:111], v[0:7], v[40:47], v[108:111], v252, v251 op_sel_hi:[0,0,0]
	v_mfma_scale_f32_16x16x128_f8f6f4 v[104:107], v[8:15], v[40:47], v[104:107], v252, v251 op_sel_hi:[0,0,0]
	v_mfma_scale_f32_16x16x128_f8f6f4 v[92:95], v[0:7], v[48:55], v[92:95], v252, v251 op_sel_hi:[0,0,0]
	v_mfma_scale_f32_16x16x128_f8f6f4 v[88:91], v[8:15], v[48:55], v[88:91], v252, v251 op_sel_hi:[0,0,0]
	v_mfma_scale_f32_16x16x128_f8f6f4 v[76:79], v[0:7], v[56:63], v[76:79], v252, v251 op_sel_hi:[0,0,0]
	v_mfma_scale_f32_16x16x128_f8f6f4 v[72:75], v[8:15], v[56:63], v[72:75], v252, v251 op_sel_hi:[0,0,0]
	s_setprio 0
	s_setprio 1
	v_mfma_scale_f32_16x16x128_f8f6f4 v[116:119], v[16:23], v[32:39], v[116:119], v252, v251 op_sel_hi:[0,0,0]
	v_mfma_scale_f32_16x16x128_f8f6f4 v[112:115], v[24:31], v[32:39], v[112:115], v252, v251 op_sel_hi:[0,0,0]
	v_mfma_scale_f32_16x16x128_f8f6f4 v[100:103], v[16:23], v[40:47], v[100:103], v252, v251 op_sel_hi:[0,0,0]
	v_mfma_scale_f32_16x16x128_f8f6f4 v[96:99], v[24:31], v[40:47], v[96:99], v252, v251 op_sel_hi:[0,0,0]
	v_mfma_scale_f32_16x16x128_f8f6f4 v[84:87], v[16:23], v[48:55], v[84:87], v252, v251 op_sel_hi:[0,0,0]
	v_mfma_scale_f32_16x16x128_f8f6f4 v[80:83], v[24:31], v[48:55], v[80:83], v252, v251 op_sel_hi:[0,0,0]
	v_mfma_scale_f32_16x16x128_f8f6f4 v[68:71], v[16:23], v[56:63], v[68:71], v252, v251 op_sel_hi:[0,0,0]
	v_mfma_scale_f32_16x16x128_f8f6f4 v[64:67], v[24:31], v[56:63], v[64:67], v252, v251 op_sel_hi:[0,0,0]
	s_setprio 0
	s_barrier
	s_mov_b64 s[84:85], 0
	s_mov_b64 s[80:81], -1
	s_and_b64 vcc, exec, s[50:51]
	s_cbranch_vccnz .LBB0_1160
	s_mov_b64 s[82:83], 0x100
	s_branch .LBB0_1155
